# GEMM K-loops: back-edge rotation - induction updates, loop test and the head's address selection moved in front of the loop-back barrier
# baseline (speedup 1.0000x reference)
.Lmy_kl_398:
	ds_read_b128 v[146:149], v142
	ds_read_b128 v[150:153], v142 offset:1024
	ds_read_b128 v[154:157], v142 offset:2048
	ds_read_b128 v[158:161], v142 offset:3072
	ds_read_b128 v[162:165], v142 offset:16384
	ds_read_b128 v[166:169], v142 offset:17408
	ds_read_b128 v[170:173], v142 offset:18432
	ds_read_b128 v[178:181], v142 offset:19456
	v_lshl_add_u64 v[174:175], s[46:47], 0, v[138:139]
	s_add_i32 m0, s56, 0xc000
	ds_read_b128 v[182:185], v145
	ds_read_b128 v[186:189], v145 offset:1024
	ds_read_b128 v[190:193], v145 offset:2048
	ds_read_b128 v[194:197], v145 offset:3072
	ds_read_b128 v[198:201], v145 offset:4096
	ds_read_b128 v[202:205], v145 offset:5120
	ds_read_b128 v[206:209], v145 offset:6144
	ds_read_b128 v[226:229], v145 offset:7168
	global_load_lds_dwordx4 v[174:175], off
	v_lshl_add_u64 v[174:175], s[46:47], 0, v[140:141]
	s_add_i32 m0, s56, 0xe000
	s_nop 0
	global_load_lds_dwordx4 v[174:175], off
	s_waitcnt vmcnt(8)
	s_waitcnt lgkmcnt(0)
	s_barrier
	s_setprio 1
	s_waitcnt lgkmcnt(0)
	v_mfma_f32_16x16x32_bf16 v[128:131], v[146:149], v[182:185], v[128:131]
	v_mfma_f32_16x16x32_bf16 v[124:127], v[154:157], v[182:185], v[124:127]
	v_mfma_f32_16x16x32_bf16 v[120:123], v[146:149], v[190:193], v[120:123]
	v_mfma_f32_16x16x32_bf16 v[116:119], v[154:157], v[190:193], v[116:119]
	v_mfma_f32_16x16x32_bf16 v[104:107], v[146:149], v[198:201], v[104:107]
	v_mfma_f32_16x16x32_bf16 v[100:103], v[154:157], v[198:201], v[100:103]
	v_mfma_f32_16x16x32_bf16 v[88:91], v[146:149], v[206:209], v[88:91]
	v_mfma_f32_16x16x32_bf16 v[84:87], v[154:157], v[206:209], v[84:87]
	v_mfma_f32_16x16x32_bf16 v[128:131], v[150:153], v[186:189], v[128:131]
	v_mfma_f32_16x16x32_bf16 v[124:127], v[158:161], v[186:189], v[124:127]
	v_mfma_f32_16x16x32_bf16 v[120:123], v[150:153], v[194:197], v[120:123]
	v_mfma_f32_16x16x32_bf16 v[116:119], v[158:161], v[194:197], v[116:119]
	v_mfma_f32_16x16x32_bf16 v[104:107], v[150:153], v[202:205], v[104:107]
	v_mfma_f32_16x16x32_bf16 v[100:103], v[158:161], v[202:205], v[100:103]
	v_mfma_f32_16x16x32_bf16 v[88:91], v[150:153], v[226:229], v[88:91]
	v_mfma_f32_16x16x32_bf16 v[84:87], v[158:161], v[226:229], v[84:87]
	s_setprio 0
	s_setprio 1
	v_mfma_f32_16x16x32_bf16 v[112:115], v[162:165], v[182:185], v[112:115]
	v_mfma_f32_16x16x32_bf16 v[108:111], v[170:173], v[182:185], v[108:111]
	v_mfma_f32_16x16x32_bf16 v[96:99], v[162:165], v[190:193], v[96:99]
	v_mfma_f32_16x16x32_bf16 v[92:95], v[170:173], v[190:193], v[92:95]
	v_mfma_f32_16x16x32_bf16 v[80:83], v[162:165], v[198:201], v[80:83]
	v_mfma_f32_16x16x32_bf16 v[76:79], v[170:173], v[198:201], v[76:79]
	v_mfma_f32_16x16x32_bf16 v[72:75], v[162:165], v[206:209], v[72:75]
	v_mfma_f32_16x16x32_bf16 v[68:71], v[170:173], v[206:209], v[68:71]
	v_mfma_f32_16x16x32_bf16 v[112:115], v[166:169], v[186:189], v[112:115]
	v_mfma_f32_16x16x32_bf16 v[108:111], v[178:181], v[186:189], v[108:111]
	v_mfma_f32_16x16x32_bf16 v[96:99], v[166:169], v[194:197], v[96:99]
	v_mfma_f32_16x16x32_bf16 v[92:95], v[178:181], v[194:197], v[92:95]
	v_mfma_f32_16x16x32_bf16 v[80:83], v[166:169], v[202:205], v[80:83]
	v_mfma_f32_16x16x32_bf16 v[76:79], v[178:181], v[202:205], v[76:79]
	v_mfma_f32_16x16x32_bf16 v[72:75], v[166:169], v[226:229], v[72:75]
	v_mfma_f32_16x16x32_bf16 v[68:71], v[178:181], v[226:229], v[68:71]
	s_setprio 0
	s_barrier
	s_add_i32 s68, s68, s55
	v_lshl_add_u64 v[174:175], s[48:49], 0, v[2:3]
	s_mov_b32 m0, s68
	ds_read_b128 v[182:185], v145 offset:16384
	ds_read_b128 v[186:189], v145 offset:17408
	ds_read_b128 v[190:193], v145 offset:18432
	ds_read_b128 v[194:197], v145 offset:19456
	ds_read_b128 v[198:201], v145 offset:20480
	ds_read_b128 v[202:205], v145 offset:21504
	ds_read_b128 v[206:209], v145 offset:22528
	ds_read_b128 v[226:229], v145 offset:23552
	global_load_lds_dwordx4 v[174:175], off
	s_add_i32 m0, s68, 0x2000
	s_add_u32 s68, s48, 0x80000
	v_lshl_add_u64 v[210:211], s[48:49], 0, v[132:133]
	s_addc_u32 s69, s49, 0
	s_add_i32 s70, s70, s55
	global_load_lds_dwordx4 v[210:211], off
	v_lshl_add_u64 v[214:215], s[68:69], 0, v[2:3]
	s_mov_b32 m0, s70
	v_lshl_add_u64 v[230:231], s[52:53], 0, v[134:135]
	global_load_lds_dwordx4 v[214:215], off
	v_lshl_add_u64 v[214:215], s[68:69], 0, v[132:133]
	s_add_i32 m0, s70, 0x2000
	s_nop 0
	global_load_lds_dwordx4 v[214:215], off
	v_lshl_add_u64 v[214:215], s[52:53], 0, v[136:137]
	s_mov_b32 m0, s56
	s_nop 0
	global_load_lds_dwordx4 v[214:215], off
	s_mov_b32 m0, s57
	s_nop 0
	global_load_lds_dwordx4 v[230:231], off
	s_waitcnt vmcnt(8)
	s_waitcnt lgkmcnt(0)
	s_barrier
	s_setprio 1
	s_waitcnt lgkmcnt(0)
	v_mfma_f32_16x16x32_bf16 v[64:67], v[146:149], v[182:185], v[64:67]
	v_mfma_f32_16x16x32_bf16 v[60:63], v[154:157], v[182:185], v[60:63]
	v_mfma_f32_16x16x32_bf16 v[56:59], v[146:149], v[190:193], v[56:59]
	v_mfma_f32_16x16x32_bf16 v[52:55], v[154:157], v[190:193], v[52:55]
	v_mfma_f32_16x16x32_bf16 v[40:43], v[146:149], v[198:201], v[40:43]
	v_mfma_f32_16x16x32_bf16 v[36:39], v[154:157], v[198:201], v[36:39]
	v_mfma_f32_16x16x32_bf16 v[24:27], v[146:149], v[206:209], v[24:27]
	v_mfma_f32_16x16x32_bf16 v[20:23], v[154:157], v[206:209], v[20:23]
	v_mfma_f32_16x16x32_bf16 v[64:67], v[150:153], v[186:189], v[64:67]
	v_mfma_f32_16x16x32_bf16 v[60:63], v[158:161], v[186:189], v[60:63]
	v_mfma_f32_16x16x32_bf16 v[56:59], v[150:153], v[194:197], v[56:59]
	v_mfma_f32_16x16x32_bf16 v[52:55], v[158:161], v[194:197], v[52:55]
	v_mfma_f32_16x16x32_bf16 v[40:43], v[150:153], v[202:205], v[40:43]
	v_mfma_f32_16x16x32_bf16 v[36:39], v[158:161], v[202:205], v[36:39]
	v_mfma_f32_16x16x32_bf16 v[24:27], v[150:153], v[226:229], v[24:27]
	v_mfma_f32_16x16x32_bf16 v[20:23], v[158:161], v[226:229], v[20:23]
	s_setprio 0
	s_setprio 1
	v_mfma_f32_16x16x32_bf16 v[48:51], v[162:165], v[182:185], v[48:51]
	v_mfma_f32_16x16x32_bf16 v[44:47], v[170:173], v[182:185], v[44:47]
	v_mfma_f32_16x16x32_bf16 v[32:35], v[162:165], v[190:193], v[32:35]
	v_mfma_f32_16x16x32_bf16 v[28:31], v[170:173], v[190:193], v[28:31]
	v_mfma_f32_16x16x32_bf16 v[16:19], v[162:165], v[198:201], v[16:19]
	v_mfma_f32_16x16x32_bf16 v[12:15], v[170:173], v[198:201], v[12:15]
	v_mfma_f32_16x16x32_bf16 v[8:11], v[162:165], v[206:209], v[8:11]
	v_mfma_f32_16x16x32_bf16 v[4:7], v[170:173], v[206:209], v[4:7]
	v_mfma_f32_16x16x32_bf16 v[48:51], v[166:169], v[186:189], v[48:51]
	v_mfma_f32_16x16x32_bf16 v[44:47], v[178:181], v[186:189], v[44:47]
	v_mfma_f32_16x16x32_bf16 v[32:35], v[166:169], v[194:197], v[32:35]
	v_mfma_f32_16x16x32_bf16 v[28:31], v[178:181], v[194:197], v[28:31]
	v_mfma_f32_16x16x32_bf16 v[16:19], v[166:169], v[202:205], v[16:19]
	v_mfma_f32_16x16x32_bf16 v[12:15], v[178:181], v[202:205], v[12:15]
	v_mfma_f32_16x16x32_bf16 v[8:11], v[166:169], v[226:229], v[8:11]
	v_mfma_f32_16x16x32_bf16 v[4:7], v[178:181], v[226:229], v[4:7]
	s_setprio 0
	s_barrier
	s_add_i32 s68, 0, 0x18000
	s_add_i32 s69, 0, 0x1c000
	ds_read_b128 v[146:149], v142 offset:32768
	ds_read_b128 v[150:153], v142 offset:33792
	ds_read_b128 v[154:157], v142 offset:34816
	ds_read_b128 v[158:161], v142 offset:35840
	ds_read_b128 v[162:165], v142 offset:49152
	ds_read_b128 v[166:169], v142 offset:50176
	ds_read_b128 v[170:173], v142 offset:51200
	ds_read_b128 v[178:181], v142 offset:52224
	s_add_u32 s52, s52, 0x80000
	s_addc_u32 s53, s53, 0
	s_mov_b32 m0, s58
	v_lshl_add_u64 v[232:233], s[52:53], 0, v[136:137]
	ds_read_b128 v[182:185], v145 offset:32768
	ds_read_b128 v[186:189], v145 offset:33792
	ds_read_b128 v[190:193], v145 offset:34816
	ds_read_b128 v[194:197], v145 offset:35840
	ds_read_b128 v[198:201], v145 offset:36864
	ds_read_b128 v[202:205], v145 offset:37888
	ds_read_b128 v[206:209], v145 offset:38912
	ds_read_b128 v[226:229], v145 offset:39936
	global_load_lds_dwordx4 v[232:233], off
	v_lshl_add_u64 v[232:233], s[52:53], 0, v[134:135]
	s_mov_b32 m0, s59
	s_nop 0
	global_load_lds_dwordx4 v[232:233], off
	s_waitcnt vmcnt(8)
	s_waitcnt lgkmcnt(0)
	s_barrier
	s_setprio 1
	s_waitcnt lgkmcnt(0)
	v_mfma_f32_16x16x32_bf16 v[128:131], v[146:149], v[182:185], v[128:131]
	v_mfma_f32_16x16x32_bf16 v[124:127], v[154:157], v[182:185], v[124:127]
	v_mfma_f32_16x16x32_bf16 v[120:123], v[146:149], v[190:193], v[120:123]
	v_mfma_f32_16x16x32_bf16 v[116:119], v[154:157], v[190:193], v[116:119]
	v_mfma_f32_16x16x32_bf16 v[104:107], v[146:149], v[198:201], v[104:107]
	v_mfma_f32_16x16x32_bf16 v[100:103], v[154:157], v[198:201], v[100:103]
	v_mfma_f32_16x16x32_bf16 v[88:91], v[146:149], v[206:209], v[88:91]
	v_mfma_f32_16x16x32_bf16 v[84:87], v[154:157], v[206:209], v[84:87]
	v_mfma_f32_16x16x32_bf16 v[128:131], v[150:153], v[186:189], v[128:131]
	v_mfma_f32_16x16x32_bf16 v[124:127], v[158:161], v[186:189], v[124:127]
	v_mfma_f32_16x16x32_bf16 v[120:123], v[150:153], v[194:197], v[120:123]
	v_mfma_f32_16x16x32_bf16 v[116:119], v[158:161], v[194:197], v[116:119]
	v_mfma_f32_16x16x32_bf16 v[104:107], v[150:153], v[202:205], v[104:107]
	v_mfma_f32_16x16x32_bf16 v[100:103], v[158:161], v[202:205], v[100:103]
	v_mfma_f32_16x16x32_bf16 v[88:91], v[150:153], v[226:229], v[88:91]
	v_mfma_f32_16x16x32_bf16 v[84:87], v[158:161], v[226:229], v[84:87]
	s_setprio 0
	s_setprio 1
	v_mfma_f32_16x16x32_bf16 v[112:115], v[162:165], v[182:185], v[112:115]
	v_mfma_f32_16x16x32_bf16 v[108:111], v[170:173], v[182:185], v[108:111]
	v_mfma_f32_16x16x32_bf16 v[96:99], v[162:165], v[190:193], v[96:99]
	v_mfma_f32_16x16x32_bf16 v[92:95], v[170:173], v[190:193], v[92:95]
	v_mfma_f32_16x16x32_bf16 v[80:83], v[162:165], v[198:201], v[80:83]
	v_mfma_f32_16x16x32_bf16 v[76:79], v[170:173], v[198:201], v[76:79]
	v_mfma_f32_16x16x32_bf16 v[72:75], v[162:165], v[206:209], v[72:75]
	v_mfma_f32_16x16x32_bf16 v[68:71], v[170:173], v[206:209], v[68:71]
	v_mfma_f32_16x16x32_bf16 v[112:115], v[166:169], v[186:189], v[112:115]
	v_mfma_f32_16x16x32_bf16 v[108:111], v[178:181], v[186:189], v[108:111]
	v_mfma_f32_16x16x32_bf16 v[96:99], v[166:169], v[194:197], v[96:99]
	v_mfma_f32_16x16x32_bf16 v[92:95], v[178:181], v[194:197], v[92:95]
	v_mfma_f32_16x16x32_bf16 v[80:83], v[166:169], v[202:205], v[80:83]
	v_mfma_f32_16x16x32_bf16 v[76:79], v[178:181], v[202:205], v[76:79]
	v_mfma_f32_16x16x32_bf16 v[72:75], v[166:169], v[226:229], v[72:75]
	v_mfma_f32_16x16x32_bf16 v[68:71], v[178:181], v[226:229], v[68:71]
	s_setprio 0
	s_barrier
	s_add_i32 s52, s68, s55
	v_lshl_add_u64 v[174:175], v[174:175], 0, s[6:7]
	s_mov_b32 m0, s52
	ds_read_b128 v[182:185], v145 offset:49152
	ds_read_b128 v[186:189], v145 offset:50176
	ds_read_b128 v[190:193], v145 offset:51200
	ds_read_b128 v[194:197], v145 offset:52224
	ds_read_b128 v[198:201], v145 offset:53248
	ds_read_b128 v[202:205], v145 offset:54272
	ds_read_b128 v[206:209], v145 offset:55296
	ds_read_b128 v[226:229], v145 offset:56320
	global_load_lds_dwordx4 v[174:175], off
	s_add_i32 m0, s52, 0x2000
	s_add_u32 s48, s48, 0x80080
	v_lshl_add_u64 v[174:175], v[210:211], 0, s[6:7]
	s_addc_u32 s49, s49, 0
	s_add_i32 s52, s69, s55
	global_load_lds_dwordx4 v[174:175], off
	v_lshl_add_u64 v[174:175], s[48:49], 0, v[2:3]
	s_mov_b32 m0, s52
	s_nop 0
	global_load_lds_dwordx4 v[174:175], off
	v_lshl_add_u64 v[174:175], s[48:49], 0, v[132:133]
	s_add_i32 m0, s52, 0x2000
	s_nop 0
	global_load_lds_dwordx4 v[174:175], off
	v_lshl_add_u64 v[174:175], v[214:215], 0, s[6:7]
	s_mov_b32 m0, s60
	s_nop 0
	global_load_lds_dwordx4 v[174:175], off
	v_lshl_add_u64 v[174:175], v[230:231], 0, s[6:7]
	s_mov_b32 m0, s61
	s_nop 0
	global_load_lds_dwordx4 v[174:175], off
	s_waitcnt vmcnt(8)
	s_waitcnt lgkmcnt(0)
	s_barrier
	s_setprio 1
	s_waitcnt lgkmcnt(0)
	v_mfma_f32_16x16x32_bf16 v[64:67], v[146:149], v[182:185], v[64:67]
	v_mfma_f32_16x16x32_bf16 v[60:63], v[154:157], v[182:185], v[60:63]
	v_mfma_f32_16x16x32_bf16 v[56:59], v[146:149], v[190:193], v[56:59]
	v_mfma_f32_16x16x32_bf16 v[52:55], v[154:157], v[190:193], v[52:55]
	v_mfma_f32_16x16x32_bf16 v[40:43], v[146:149], v[198:201], v[40:43]
	v_mfma_f32_16x16x32_bf16 v[36:39], v[154:157], v[198:201], v[36:39]
	v_mfma_f32_16x16x32_bf16 v[24:27], v[146:149], v[206:209], v[24:27]
	v_mfma_f32_16x16x32_bf16 v[20:23], v[154:157], v[206:209], v[20:23]
	v_mfma_f32_16x16x32_bf16 v[64:67], v[150:153], v[186:189], v[64:67]
	v_mfma_f32_16x16x32_bf16 v[60:63], v[158:161], v[186:189], v[60:63]
	v_mfma_f32_16x16x32_bf16 v[56:59], v[150:153], v[194:197], v[56:59]
	v_mfma_f32_16x16x32_bf16 v[52:55], v[158:161], v[194:197], v[52:55]
	v_mfma_f32_16x16x32_bf16 v[40:43], v[150:153], v[202:205], v[40:43]
	v_mfma_f32_16x16x32_bf16 v[36:39], v[158:161], v[202:205], v[36:39]
	v_mfma_f32_16x16x32_bf16 v[24:27], v[150:153], v[226:229], v[24:27]
	v_mfma_f32_16x16x32_bf16 v[20:23], v[158:161], v[226:229], v[20:23]
	s_setprio 0
	s_setprio 1
	v_mfma_f32_16x16x32_bf16 v[48:51], v[162:165], v[182:185], v[48:51]
	v_mfma_f32_16x16x32_bf16 v[44:47], v[170:173], v[182:185], v[44:47]
	v_mfma_f32_16x16x32_bf16 v[32:35], v[162:165], v[190:193], v[32:35]
	v_mfma_f32_16x16x32_bf16 v[28:31], v[170:173], v[190:193], v[28:31]
	v_mfma_f32_16x16x32_bf16 v[16:19], v[162:165], v[198:201], v[16:19]
	v_mfma_f32_16x16x32_bf16 v[12:15], v[170:173], v[198:201], v[12:15]
	v_mfma_f32_16x16x32_bf16 v[8:11], v[162:165], v[206:209], v[8:11]
	v_mfma_f32_16x16x32_bf16 v[4:7], v[170:173], v[206:209], v[4:7]
	v_mfma_f32_16x16x32_bf16 v[48:51], v[166:169], v[186:189], v[48:51]
	v_mfma_f32_16x16x32_bf16 v[44:47], v[178:181], v[186:189], v[44:47]
	v_mfma_f32_16x16x32_bf16 v[32:35], v[166:169], v[194:197], v[32:35]
	v_mfma_f32_16x16x32_bf16 v[28:31], v[178:181], v[194:197], v[28:31]
	v_mfma_f32_16x16x32_bf16 v[16:19], v[166:169], v[202:205], v[16:19]
	v_mfma_f32_16x16x32_bf16 v[12:15], v[178:181], v[202:205], v[12:15]
	v_mfma_f32_16x16x32_bf16 v[8:11], v[166:169], v[226:229], v[8:11]
	v_mfma_f32_16x16x32_bf16 v[4:7], v[178:181], v[226:229], v[4:7]
	s_setprio 0
	s_add_i32 s67, s67, 2
	s_add_u32 s46, s46, 0x100
	s_addc_u32 s47, s47, 0
	s_add_u32 s65, s65, 0x100
	s_addc_u32 s66, s66, 0
	s_cmp_gt_u32 s67, 29
	s_cbranch_scc1 .Lmy_kx_398
	s_add_u32 s48, s46, 0xfff80080
	s_addc_u32 s49, s47, -1
	s_add_i32 s68, 0, 0x10000
	s_cmp_eq_u32 s67, 28
	s_cselect_b32 s53, s10, s49
	s_cselect_b32 s52, s11, s48
	s_cselect_b32 s49, s39, s66
	s_cselect_b32 s48, s41, s65
	s_add_i32 s70, 0, 0x14000
	s_cmp_gt_u32 s67, 29
.Lmy_kx_398:
	s_barrier
	s_cbranch_scc0 .Lmy_kl_398
	s_and_b64 vcc, exec, s[36:37]
	s_cbranch_vccz .LBB0_401
	s_barrier

.Lmy_kl_585:
	ds_read_b128 v[146:149], v142
	ds_read_b128 v[150:153], v142 offset:1024
	ds_read_b128 v[154:157], v142 offset:2048
	ds_read_b128 v[158:161], v142 offset:3072
	ds_read_b128 v[162:165], v142 offset:16384
	ds_read_b128 v[166:169], v142 offset:17408
	ds_read_b128 v[170:173], v142 offset:18432
	ds_read_b128 v[178:181], v142 offset:19456
	v_lshl_add_u64 v[174:175], s[56:57], 0, v[138:139]
	s_add_i32 m0, s39, 0xc000
	ds_read_b128 v[182:185], v145
	ds_read_b128 v[186:189], v145 offset:1024
	ds_read_b128 v[190:193], v145 offset:2048
	ds_read_b128 v[194:197], v145 offset:3072
	ds_read_b128 v[198:201], v145 offset:4096
	ds_read_b128 v[202:205], v145 offset:5120
	ds_read_b128 v[206:209], v145 offset:6144
	ds_read_b128 v[226:229], v145 offset:7168
	global_load_lds_dwordx4 v[174:175], off
	v_lshl_add_u64 v[174:175], s[56:57], 0, v[140:141]
	s_add_i32 m0, s39, 0xe000
	s_nop 0
	global_load_lds_dwordx4 v[174:175], off
	s_waitcnt vmcnt(8)
	s_waitcnt lgkmcnt(0)
	s_barrier
	s_setprio 1
	s_waitcnt lgkmcnt(0)
	v_mfma_f32_16x16x32_bf16 v[128:131], v[146:149], v[182:185], v[128:131]
	v_mfma_f32_16x16x32_bf16 v[124:127], v[154:157], v[182:185], v[124:127]
	v_mfma_f32_16x16x32_bf16 v[120:123], v[146:149], v[190:193], v[120:123]
	v_mfma_f32_16x16x32_bf16 v[116:119], v[154:157], v[190:193], v[116:119]
	v_mfma_f32_16x16x32_bf16 v[104:107], v[146:149], v[198:201], v[104:107]
	v_mfma_f32_16x16x32_bf16 v[100:103], v[154:157], v[198:201], v[100:103]
	v_mfma_f32_16x16x32_bf16 v[88:91], v[146:149], v[206:209], v[88:91]
	v_mfma_f32_16x16x32_bf16 v[84:87], v[154:157], v[206:209], v[84:87]
	v_mfma_f32_16x16x32_bf16 v[128:131], v[150:153], v[186:189], v[128:131]
	v_mfma_f32_16x16x32_bf16 v[124:127], v[158:161], v[186:189], v[124:127]
	v_mfma_f32_16x16x32_bf16 v[120:123], v[150:153], v[194:197], v[120:123]
	v_mfma_f32_16x16x32_bf16 v[116:119], v[158:161], v[194:197], v[116:119]
	v_mfma_f32_16x16x32_bf16 v[104:107], v[150:153], v[202:205], v[104:107]
	v_mfma_f32_16x16x32_bf16 v[100:103], v[158:161], v[202:205], v[100:103]
	v_mfma_f32_16x16x32_bf16 v[88:91], v[150:153], v[226:229], v[88:91]
	v_mfma_f32_16x16x32_bf16 v[84:87], v[158:161], v[226:229], v[84:87]
	s_setprio 0
	s_setprio 1
	v_mfma_f32_16x16x32_bf16 v[112:115], v[162:165], v[182:185], v[112:115]
	v_mfma_f32_16x16x32_bf16 v[108:111], v[170:173], v[182:185], v[108:111]
	v_mfma_f32_16x16x32_bf16 v[96:99], v[162:165], v[190:193], v[96:99]
	v_mfma_f32_16x16x32_bf16 v[92:95], v[170:173], v[190:193], v[92:95]
	v_mfma_f32_16x16x32_bf16 v[80:83], v[162:165], v[198:201], v[80:83]
	v_mfma_f32_16x16x32_bf16 v[76:79], v[170:173], v[198:201], v[76:79]
	v_mfma_f32_16x16x32_bf16 v[72:75], v[162:165], v[206:209], v[72:75]
	v_mfma_f32_16x16x32_bf16 v[68:71], v[170:173], v[206:209], v[68:71]
	v_mfma_f32_16x16x32_bf16 v[112:115], v[166:169], v[186:189], v[112:115]
	v_mfma_f32_16x16x32_bf16 v[108:111], v[178:181], v[186:189], v[108:111]
	v_mfma_f32_16x16x32_bf16 v[96:99], v[166:169], v[194:197], v[96:99]
	v_mfma_f32_16x16x32_bf16 v[92:95], v[178:181], v[194:197], v[92:95]
	v_mfma_f32_16x16x32_bf16 v[80:83], v[166:169], v[202:205], v[80:83]
	v_mfma_f32_16x16x32_bf16 v[76:79], v[178:181], v[202:205], v[76:79]
	v_mfma_f32_16x16x32_bf16 v[72:75], v[166:169], v[226:229], v[72:75]
	v_mfma_f32_16x16x32_bf16 v[68:71], v[178:181], v[226:229], v[68:71]
	s_setprio 0
	s_barrier
	s_add_i32 s42, s76, s67
	v_lshl_add_u64 v[174:175], s[58:59], 0, v[2:3]
	s_mov_b32 m0, s42
	ds_read_b128 v[182:185], v145 offset:16384
	ds_read_b128 v[186:189], v145 offset:17408
	ds_read_b128 v[190:193], v145 offset:18432
	ds_read_b128 v[194:197], v145 offset:19456
	ds_read_b128 v[198:201], v145 offset:20480
	ds_read_b128 v[202:205], v145 offset:21504
	ds_read_b128 v[206:209], v145 offset:22528
	ds_read_b128 v[226:229], v145 offset:23552
	global_load_lds_dwordx4 v[174:175], off
	s_add_i32 m0, s42, 0x2000
	s_add_u32 s42, s58, 0x20000
	v_lshl_add_u64 v[210:211], s[58:59], 0, v[132:133]
	s_addc_u32 s43, s59, 0
	s_add_i32 s76, s77, s67
	global_load_lds_dwordx4 v[210:211], off
	v_lshl_add_u64 v[214:215], s[42:43], 0, v[2:3]
	s_mov_b32 m0, s76
	v_lshl_add_u64 v[230:231], s[60:61], 0, v[134:135]
	global_load_lds_dwordx4 v[214:215], off
	v_lshl_add_u64 v[214:215], s[42:43], 0, v[132:133]
	s_add_i32 m0, s76, 0x2000
	s_nop 0
	global_load_lds_dwordx4 v[214:215], off
	v_lshl_add_u64 v[214:215], s[60:61], 0, v[136:137]
	s_mov_b32 m0, s39
	s_nop 0
	global_load_lds_dwordx4 v[214:215], off
	s_mov_b32 m0, s41
	s_nop 0
	global_load_lds_dwordx4 v[230:231], off
	s_waitcnt vmcnt(8)
	s_waitcnt lgkmcnt(0)
	s_barrier
	s_setprio 1
	s_waitcnt lgkmcnt(0)
	v_mfma_f32_16x16x32_bf16 v[64:67], v[146:149], v[182:185], v[64:67]
	v_mfma_f32_16x16x32_bf16 v[60:63], v[154:157], v[182:185], v[60:63]
	v_mfma_f32_16x16x32_bf16 v[56:59], v[146:149], v[190:193], v[56:59]
	v_mfma_f32_16x16x32_bf16 v[52:55], v[154:157], v[190:193], v[52:55]
	v_mfma_f32_16x16x32_bf16 v[40:43], v[146:149], v[198:201], v[40:43]
	v_mfma_f32_16x16x32_bf16 v[36:39], v[154:157], v[198:201], v[36:39]
	v_mfma_f32_16x16x32_bf16 v[24:27], v[146:149], v[206:209], v[24:27]
	v_mfma_f32_16x16x32_bf16 v[20:23], v[154:157], v[206:209], v[20:23]
	v_mfma_f32_16x16x32_bf16 v[64:67], v[150:153], v[186:189], v[64:67]
	v_mfma_f32_16x16x32_bf16 v[60:63], v[158:161], v[186:189], v[60:63]
	v_mfma_f32_16x16x32_bf16 v[56:59], v[150:153], v[194:197], v[56:59]
	v_mfma_f32_16x16x32_bf16 v[52:55], v[158:161], v[194:197], v[52:55]
	v_mfma_f32_16x16x32_bf16 v[40:43], v[150:153], v[202:205], v[40:43]
	v_mfma_f32_16x16x32_bf16 v[36:39], v[158:161], v[202:205], v[36:39]
	v_mfma_f32_16x16x32_bf16 v[24:27], v[150:153], v[226:229], v[24:27]
	v_mfma_f32_16x16x32_bf16 v[20:23], v[158:161], v[226:229], v[20:23]
	s_setprio 0
	s_setprio 1
	v_mfma_f32_16x16x32_bf16 v[48:51], v[162:165], v[182:185], v[48:51]
	v_mfma_f32_16x16x32_bf16 v[44:47], v[170:173], v[182:185], v[44:47]
	v_mfma_f32_16x16x32_bf16 v[32:35], v[162:165], v[190:193], v[32:35]
	v_mfma_f32_16x16x32_bf16 v[28:31], v[170:173], v[190:193], v[28:31]
	v_mfma_f32_16x16x32_bf16 v[16:19], v[162:165], v[198:201], v[16:19]
	v_mfma_f32_16x16x32_bf16 v[12:15], v[170:173], v[198:201], v[12:15]
	v_mfma_f32_16x16x32_bf16 v[8:11], v[162:165], v[206:209], v[8:11]
	v_mfma_f32_16x16x32_bf16 v[4:7], v[170:173], v[206:209], v[4:7]
	v_mfma_f32_16x16x32_bf16 v[48:51], v[166:169], v[186:189], v[48:51]
	v_mfma_f32_16x16x32_bf16 v[44:47], v[178:181], v[186:189], v[44:47]
	v_mfma_f32_16x16x32_bf16 v[32:35], v[166:169], v[194:197], v[32:35]
	v_mfma_f32_16x16x32_bf16 v[28:31], v[178:181], v[194:197], v[28:31]
	v_mfma_f32_16x16x32_bf16 v[16:19], v[166:169], v[202:205], v[16:19]
	v_mfma_f32_16x16x32_bf16 v[12:15], v[178:181], v[202:205], v[12:15]
	v_mfma_f32_16x16x32_bf16 v[8:11], v[166:169], v[226:229], v[8:11]
	v_mfma_f32_16x16x32_bf16 v[4:7], v[178:181], v[226:229], v[4:7]
	s_setprio 0
	s_barrier
	s_add_i32 s76, 0, 0x18000
	s_add_i32 s77, 0, 0x1c000
	ds_read_b128 v[146:149], v142 offset:32768
	ds_read_b128 v[150:153], v142 offset:33792
	ds_read_b128 v[154:157], v142 offset:34816
	ds_read_b128 v[158:161], v142 offset:35840
	ds_read_b128 v[162:165], v142 offset:49152
	ds_read_b128 v[166:169], v142 offset:50176
	ds_read_b128 v[170:173], v142 offset:51200
	ds_read_b128 v[178:181], v142 offset:52224
	s_add_u32 s42, s60, 0x20000
	s_addc_u32 s43, s61, 0
	s_mov_b32 m0, s68
	v_lshl_add_u64 v[232:233], s[42:43], 0, v[136:137]
	ds_read_b128 v[182:185], v145 offset:32768
	ds_read_b128 v[186:189], v145 offset:33792
	ds_read_b128 v[190:193], v145 offset:34816
	ds_read_b128 v[194:197], v145 offset:35840
	ds_read_b128 v[198:201], v145 offset:36864
	ds_read_b128 v[202:205], v145 offset:37888
	ds_read_b128 v[206:209], v145 offset:38912
	ds_read_b128 v[226:229], v145 offset:39936
	global_load_lds_dwordx4 v[232:233], off
	v_lshl_add_u64 v[232:233], s[42:43], 0, v[134:135]
	s_mov_b32 m0, s69
	s_nop 0
	global_load_lds_dwordx4 v[232:233], off
	s_waitcnt vmcnt(8)
	s_waitcnt lgkmcnt(0)
	s_barrier
	s_setprio 1
	s_waitcnt lgkmcnt(0)
	v_mfma_f32_16x16x32_bf16 v[128:131], v[146:149], v[182:185], v[128:131]
	v_mfma_f32_16x16x32_bf16 v[124:127], v[154:157], v[182:185], v[124:127]
	v_mfma_f32_16x16x32_bf16 v[120:123], v[146:149], v[190:193], v[120:123]
	v_mfma_f32_16x16x32_bf16 v[116:119], v[154:157], v[190:193], v[116:119]
	v_mfma_f32_16x16x32_bf16 v[104:107], v[146:149], v[198:201], v[104:107]
	v_mfma_f32_16x16x32_bf16 v[100:103], v[154:157], v[198:201], v[100:103]
	v_mfma_f32_16x16x32_bf16 v[88:91], v[146:149], v[206:209], v[88:91]
	v_mfma_f32_16x16x32_bf16 v[84:87], v[154:157], v[206:209], v[84:87]
	v_mfma_f32_16x16x32_bf16 v[128:131], v[150:153], v[186:189], v[128:131]
	v_mfma_f32_16x16x32_bf16 v[124:127], v[158:161], v[186:189], v[124:127]
	v_mfma_f32_16x16x32_bf16 v[120:123], v[150:153], v[194:197], v[120:123]
	v_mfma_f32_16x16x32_bf16 v[116:119], v[158:161], v[194:197], v[116:119]
	v_mfma_f32_16x16x32_bf16 v[104:107], v[150:153], v[202:205], v[104:107]
	v_mfma_f32_16x16x32_bf16 v[100:103], v[158:161], v[202:205], v[100:103]
	v_mfma_f32_16x16x32_bf16 v[88:91], v[150:153], v[226:229], v[88:91]
	v_mfma_f32_16x16x32_bf16 v[84:87], v[158:161], v[226:229], v[84:87]
	s_setprio 0
	s_setprio 1
	v_mfma_f32_16x16x32_bf16 v[112:115], v[162:165], v[182:185], v[112:115]
	v_mfma_f32_16x16x32_bf16 v[108:111], v[170:173], v[182:185], v[108:111]
	v_mfma_f32_16x16x32_bf16 v[96:99], v[162:165], v[190:193], v[96:99]
	v_mfma_f32_16x16x32_bf16 v[92:95], v[170:173], v[190:193], v[92:95]
	v_mfma_f32_16x16x32_bf16 v[80:83], v[162:165], v[198:201], v[80:83]
	v_mfma_f32_16x16x32_bf16 v[76:79], v[170:173], v[198:201], v[76:79]
	v_mfma_f32_16x16x32_bf16 v[72:75], v[162:165], v[206:209], v[72:75]
	v_mfma_f32_16x16x32_bf16 v[68:71], v[170:173], v[206:209], v[68:71]
	v_mfma_f32_16x16x32_bf16 v[112:115], v[166:169], v[186:189], v[112:115]
	v_mfma_f32_16x16x32_bf16 v[108:111], v[178:181], v[186:189], v[108:111]
	v_mfma_f32_16x16x32_bf16 v[96:99], v[166:169], v[194:197], v[96:99]
	v_mfma_f32_16x16x32_bf16 v[92:95], v[178:181], v[194:197], v[92:95]
	v_mfma_f32_16x16x32_bf16 v[80:83], v[166:169], v[202:205], v[80:83]
	v_mfma_f32_16x16x32_bf16 v[76:79], v[178:181], v[202:205], v[76:79]
	v_mfma_f32_16x16x32_bf16 v[72:75], v[166:169], v[226:229], v[72:75]
	v_mfma_f32_16x16x32_bf16 v[68:71], v[178:181], v[226:229], v[68:71]
	s_setprio 0
	s_barrier
	s_add_i32 s42, s76, s67
	v_lshl_add_u64 v[174:175], v[174:175], 0, s[6:7]
	s_mov_b32 m0, s42
	ds_read_b128 v[182:185], v145 offset:49152
	ds_read_b128 v[186:189], v145 offset:50176
	ds_read_b128 v[190:193], v145 offset:51200
	ds_read_b128 v[194:197], v145 offset:52224
	ds_read_b128 v[198:201], v145 offset:53248
	ds_read_b128 v[202:205], v145 offset:54272
	ds_read_b128 v[206:209], v145 offset:55296
	ds_read_b128 v[226:229], v145 offset:56320
	global_load_lds_dwordx4 v[174:175], off
	s_add_i32 m0, s42, 0x2000
	s_add_u32 s42, s58, 0x20080
	v_lshl_add_u64 v[174:175], v[210:211], 0, s[6:7]
	s_addc_u32 s43, s59, 0
	s_add_i32 s58, s77, s67
	global_load_lds_dwordx4 v[174:175], off
	v_lshl_add_u64 v[174:175], s[42:43], 0, v[2:3]
	s_mov_b32 m0, s58
	s_nop 0
	global_load_lds_dwordx4 v[174:175], off
	v_lshl_add_u64 v[174:175], s[42:43], 0, v[132:133]
	s_add_i32 m0, s58, 0x2000
	s_nop 0
	global_load_lds_dwordx4 v[174:175], off
	v_lshl_add_u64 v[174:175], v[214:215], 0, s[6:7]
	s_mov_b32 m0, s70
	s_nop 0
	global_load_lds_dwordx4 v[174:175], off
	v_lshl_add_u64 v[174:175], v[230:231], 0, s[6:7]
	s_mov_b32 m0, s71
	s_nop 0
	global_load_lds_dwordx4 v[174:175], off
	s_waitcnt vmcnt(8)
	s_waitcnt lgkmcnt(0)
	s_barrier
	s_setprio 1
	s_waitcnt lgkmcnt(0)
	v_mfma_f32_16x16x32_bf16 v[64:67], v[146:149], v[182:185], v[64:67]
	v_mfma_f32_16x16x32_bf16 v[60:63], v[154:157], v[182:185], v[60:63]
	v_mfma_f32_16x16x32_bf16 v[56:59], v[146:149], v[190:193], v[56:59]
	v_mfma_f32_16x16x32_bf16 v[52:55], v[154:157], v[190:193], v[52:55]
	v_mfma_f32_16x16x32_bf16 v[40:43], v[146:149], v[198:201], v[40:43]
	v_mfma_f32_16x16x32_bf16 v[36:39], v[154:157], v[198:201], v[36:39]
	v_mfma_f32_16x16x32_bf16 v[24:27], v[146:149], v[206:209], v[24:27]
	v_mfma_f32_16x16x32_bf16 v[20:23], v[154:157], v[206:209], v[20:23]
	v_mfma_f32_16x16x32_bf16 v[64:67], v[150:153], v[186:189], v[64:67]
	v_mfma_f32_16x16x32_bf16 v[60:63], v[158:161], v[186:189], v[60:63]
	v_mfma_f32_16x16x32_bf16 v[56:59], v[150:153], v[194:197], v[56:59]
	v_mfma_f32_16x16x32_bf16 v[52:55], v[158:161], v[194:197], v[52:55]
	v_mfma_f32_16x16x32_bf16 v[40:43], v[150:153], v[202:205], v[40:43]
	v_mfma_f32_16x16x32_bf16 v[36:39], v[158:161], v[202:205], v[36:39]
	v_mfma_f32_16x16x32_bf16 v[24:27], v[150:153], v[226:229], v[24:27]
	v_mfma_f32_16x16x32_bf16 v[20:23], v[158:161], v[226:229], v[20:23]
	s_setprio 0
	s_setprio 1
	v_mfma_f32_16x16x32_bf16 v[48:51], v[162:165], v[182:185], v[48:51]
	v_mfma_f32_16x16x32_bf16 v[44:47], v[170:173], v[182:185], v[44:47]
	v_mfma_f32_16x16x32_bf16 v[32:35], v[162:165], v[190:193], v[32:35]
	v_mfma_f32_16x16x32_bf16 v[28:31], v[170:173], v[190:193], v[28:31]
	v_mfma_f32_16x16x32_bf16 v[16:19], v[162:165], v[198:201], v[16:19]
	v_mfma_f32_16x16x32_bf16 v[12:15], v[170:173], v[198:201], v[12:15]
	v_mfma_f32_16x16x32_bf16 v[8:11], v[162:165], v[206:209], v[8:11]
	v_mfma_f32_16x16x32_bf16 v[4:7], v[170:173], v[206:209], v[4:7]
	v_mfma_f32_16x16x32_bf16 v[48:51], v[166:169], v[186:189], v[48:51]
	v_mfma_f32_16x16x32_bf16 v[44:47], v[178:181], v[186:189], v[44:47]
	v_mfma_f32_16x16x32_bf16 v[32:35], v[166:169], v[194:197], v[32:35]
	v_mfma_f32_16x16x32_bf16 v[28:31], v[178:181], v[194:197], v[28:31]
	v_mfma_f32_16x16x32_bf16 v[16:19], v[166:169], v[202:205], v[16:19]
	v_mfma_f32_16x16x32_bf16 v[12:15], v[178:181], v[202:205], v[12:15]
	v_mfma_f32_16x16x32_bf16 v[8:11], v[166:169], v[226:229], v[8:11]
	v_mfma_f32_16x16x32_bf16 v[4:7], v[178:181], v[226:229], v[4:7]
	s_setprio 0
	s_add_i32 s75, s75, 2
	s_add_u32 s56, s56, 0x100
	s_addc_u32 s57, s57, 0
	s_add_u32 s73, s73, 0x100
	s_addc_u32 s74, s74, 0
	s_cmp_gt_u32 s75, 5
	s_cbranch_scc1 .Lmy_kx_585
	s_add_u32 s42, s56, 0xfffe0080
	s_addc_u32 s43, s57, -1
	s_add_i32 s76, 0, 0x10000
	s_cmp_eq_u32 s75, 4
	s_cselect_b32 s61, s10, s43
	s_cselect_b32 s60, s11, s42
	s_cselect_b32 s59, s47, s74
	s_cselect_b32 s58, s49, s73
	s_add_i32 s77, 0, 0x14000
	s_cmp_gt_u32 s75, 5
.Lmy_kx_585:
	s_barrier
	s_cbranch_scc0 .Lmy_kl_585
	s_and_b64 vcc, exec, s[44:45]
	s_cbranch_vccz .LBB0_588
	s_barrier

.Lmy_kl_1427:
	ds_read_b128 v[146:149], v142
	ds_read_b128 v[150:153], v142 offset:1024
	ds_read_b128 v[154:157], v142 offset:2048
	ds_read_b128 v[158:161], v142 offset:3072
	ds_read_b128 v[162:165], v142 offset:16384
	ds_read_b128 v[166:169], v142 offset:17408
	ds_read_b128 v[170:173], v142 offset:18432
	ds_read_b128 v[178:181], v142 offset:19456
	v_lshl_add_u64 v[174:175], s[48:49], 0, v[138:139]
	s_add_i32 m0, s58, 0xc000
	ds_read_b128 v[182:185], v145
	ds_read_b128 v[186:189], v145 offset:1024
	ds_read_b128 v[190:193], v145 offset:2048
	ds_read_b128 v[194:197], v145 offset:3072
	ds_read_b128 v[198:201], v145 offset:4096
	ds_read_b128 v[202:205], v145 offset:5120
	ds_read_b128 v[206:209], v145 offset:6144
	ds_read_b128 v[226:229], v145 offset:7168
	global_load_lds_dwordx4 v[174:175], off
	v_lshl_add_u64 v[174:175], s[48:49], 0, v[140:141]
	s_add_i32 m0, s58, 0xe000
	s_nop 0
	global_load_lds_dwordx4 v[174:175], off
	s_waitcnt vmcnt(8)
	s_waitcnt lgkmcnt(0)
	s_barrier
	s_setprio 1
	s_waitcnt lgkmcnt(0)
	v_mfma_f32_16x16x32_bf16 v[128:131], v[146:149], v[182:185], v[128:131]
	v_mfma_f32_16x16x32_bf16 v[124:127], v[154:157], v[182:185], v[124:127]
	v_mfma_f32_16x16x32_bf16 v[120:123], v[146:149], v[190:193], v[120:123]
	v_mfma_f32_16x16x32_bf16 v[116:119], v[154:157], v[190:193], v[116:119]
	v_mfma_f32_16x16x32_bf16 v[104:107], v[146:149], v[198:201], v[104:107]
	v_mfma_f32_16x16x32_bf16 v[100:103], v[154:157], v[198:201], v[100:103]
	v_mfma_f32_16x16x32_bf16 v[88:91], v[146:149], v[206:209], v[88:91]
	v_mfma_f32_16x16x32_bf16 v[84:87], v[154:157], v[206:209], v[84:87]
	v_mfma_f32_16x16x32_bf16 v[128:131], v[150:153], v[186:189], v[128:131]
	v_mfma_f32_16x16x32_bf16 v[124:127], v[158:161], v[186:189], v[124:127]
	v_mfma_f32_16x16x32_bf16 v[120:123], v[150:153], v[194:197], v[120:123]
	v_mfma_f32_16x16x32_bf16 v[116:119], v[158:161], v[194:197], v[116:119]
	v_mfma_f32_16x16x32_bf16 v[104:107], v[150:153], v[202:205], v[104:107]
	v_mfma_f32_16x16x32_bf16 v[100:103], v[158:161], v[202:205], v[100:103]
	v_mfma_f32_16x16x32_bf16 v[88:91], v[150:153], v[226:229], v[88:91]
	v_mfma_f32_16x16x32_bf16 v[84:87], v[158:161], v[226:229], v[84:87]
	s_setprio 0
	s_setprio 1
	v_mfma_f32_16x16x32_bf16 v[112:115], v[162:165], v[182:185], v[112:115]
	v_mfma_f32_16x16x32_bf16 v[108:111], v[170:173], v[182:185], v[108:111]
	v_mfma_f32_16x16x32_bf16 v[96:99], v[162:165], v[190:193], v[96:99]
	v_mfma_f32_16x16x32_bf16 v[92:95], v[170:173], v[190:193], v[92:95]
	v_mfma_f32_16x16x32_bf16 v[80:83], v[162:165], v[198:201], v[80:83]
	v_mfma_f32_16x16x32_bf16 v[76:79], v[170:173], v[198:201], v[76:79]
	v_mfma_f32_16x16x32_bf16 v[72:75], v[162:165], v[206:209], v[72:75]
	v_mfma_f32_16x16x32_bf16 v[68:71], v[170:173], v[206:209], v[68:71]
	v_mfma_f32_16x16x32_bf16 v[112:115], v[166:169], v[186:189], v[112:115]
	v_mfma_f32_16x16x32_bf16 v[108:111], v[178:181], v[186:189], v[108:111]
	v_mfma_f32_16x16x32_bf16 v[96:99], v[166:169], v[194:197], v[96:99]
	v_mfma_f32_16x16x32_bf16 v[92:95], v[178:181], v[194:197], v[92:95]
	v_mfma_f32_16x16x32_bf16 v[80:83], v[166:169], v[202:205], v[80:83]
	v_mfma_f32_16x16x32_bf16 v[76:79], v[178:181], v[202:205], v[76:79]
	v_mfma_f32_16x16x32_bf16 v[72:75], v[166:169], v[226:229], v[72:75]
	v_mfma_f32_16x16x32_bf16 v[68:71], v[178:181], v[226:229], v[68:71]
	s_setprio 0
	s_barrier
	s_add_i32 s42, s70, s57
	v_lshl_add_u64 v[174:175], s[52:53], 0, v[2:3]
	s_mov_b32 m0, s42
	ds_read_b128 v[182:185], v145 offset:16384
	ds_read_b128 v[186:189], v145 offset:17408
	ds_read_b128 v[190:193], v145 offset:18432
	ds_read_b128 v[194:197], v145 offset:19456
	ds_read_b128 v[198:201], v145 offset:20480
	ds_read_b128 v[202:205], v145 offset:21504
	ds_read_b128 v[206:209], v145 offset:22528
	ds_read_b128 v[226:229], v145 offset:23552
	global_load_lds_dwordx4 v[174:175], off
	s_add_i32 m0, s42, 0x2000
	s_add_u32 s42, s52, 0x80000
	v_lshl_add_u64 v[210:211], s[52:53], 0, v[132:133]
	s_addc_u32 s43, s53, 0
	s_add_i32 s70, s71, s57
	global_load_lds_dwordx4 v[210:211], off
	v_lshl_add_u64 v[214:215], s[42:43], 0, v[2:3]
	s_mov_b32 m0, s70
	v_lshl_add_u64 v[230:231], s[54:55], 0, v[134:135]
	global_load_lds_dwordx4 v[214:215], off
	v_lshl_add_u64 v[214:215], s[42:43], 0, v[132:133]
	s_add_i32 m0, s70, 0x2000
	s_nop 0
	global_load_lds_dwordx4 v[214:215], off
	v_lshl_add_u64 v[214:215], s[54:55], 0, v[136:137]
	s_mov_b32 m0, s58
	s_nop 0
	global_load_lds_dwordx4 v[214:215], off
	s_mov_b32 m0, s59
	s_nop 0
	global_load_lds_dwordx4 v[230:231], off
	s_waitcnt vmcnt(8)
	s_waitcnt lgkmcnt(0)
	s_barrier
	s_setprio 1
	s_waitcnt lgkmcnt(0)
	v_mfma_f32_16x16x32_bf16 v[64:67], v[146:149], v[182:185], v[64:67]
	v_mfma_f32_16x16x32_bf16 v[60:63], v[154:157], v[182:185], v[60:63]
	v_mfma_f32_16x16x32_bf16 v[56:59], v[146:149], v[190:193], v[56:59]
	v_mfma_f32_16x16x32_bf16 v[52:55], v[154:157], v[190:193], v[52:55]
	v_mfma_f32_16x16x32_bf16 v[40:43], v[146:149], v[198:201], v[40:43]
	v_mfma_f32_16x16x32_bf16 v[36:39], v[154:157], v[198:201], v[36:39]
	v_mfma_f32_16x16x32_bf16 v[24:27], v[146:149], v[206:209], v[24:27]
	v_mfma_f32_16x16x32_bf16 v[20:23], v[154:157], v[206:209], v[20:23]
	v_mfma_f32_16x16x32_bf16 v[64:67], v[150:153], v[186:189], v[64:67]
	v_mfma_f32_16x16x32_bf16 v[60:63], v[158:161], v[186:189], v[60:63]
	v_mfma_f32_16x16x32_bf16 v[56:59], v[150:153], v[194:197], v[56:59]
	v_mfma_f32_16x16x32_bf16 v[52:55], v[158:161], v[194:197], v[52:55]
	v_mfma_f32_16x16x32_bf16 v[40:43], v[150:153], v[202:205], v[40:43]
	v_mfma_f32_16x16x32_bf16 v[36:39], v[158:161], v[202:205], v[36:39]
	v_mfma_f32_16x16x32_bf16 v[24:27], v[150:153], v[226:229], v[24:27]
	v_mfma_f32_16x16x32_bf16 v[20:23], v[158:161], v[226:229], v[20:23]
	s_setprio 0
	s_setprio 1
	v_mfma_f32_16x16x32_bf16 v[48:51], v[162:165], v[182:185], v[48:51]
	v_mfma_f32_16x16x32_bf16 v[44:47], v[170:173], v[182:185], v[44:47]
	v_mfma_f32_16x16x32_bf16 v[32:35], v[162:165], v[190:193], v[32:35]
	v_mfma_f32_16x16x32_bf16 v[28:31], v[170:173], v[190:193], v[28:31]
	v_mfma_f32_16x16x32_bf16 v[16:19], v[162:165], v[198:201], v[16:19]
	v_mfma_f32_16x16x32_bf16 v[12:15], v[170:173], v[198:201], v[12:15]
	v_mfma_f32_16x16x32_bf16 v[8:11], v[162:165], v[206:209], v[8:11]
	v_mfma_f32_16x16x32_bf16 v[4:7], v[170:173], v[206:209], v[4:7]
	v_mfma_f32_16x16x32_bf16 v[48:51], v[166:169], v[186:189], v[48:51]
	v_mfma_f32_16x16x32_bf16 v[44:47], v[178:181], v[186:189], v[44:47]
	v_mfma_f32_16x16x32_bf16 v[32:35], v[166:169], v[194:197], v[32:35]
	v_mfma_f32_16x16x32_bf16 v[28:31], v[178:181], v[194:197], v[28:31]
	v_mfma_f32_16x16x32_bf16 v[16:19], v[166:169], v[202:205], v[16:19]
	v_mfma_f32_16x16x32_bf16 v[12:15], v[178:181], v[202:205], v[12:15]
	v_mfma_f32_16x16x32_bf16 v[8:11], v[166:169], v[226:229], v[8:11]
	v_mfma_f32_16x16x32_bf16 v[4:7], v[178:181], v[226:229], v[4:7]
	s_setprio 0
	s_barrier
	s_add_i32 s70, 0, 0x18000
	s_add_i32 s71, 0, 0x1c000
	ds_read_b128 v[146:149], v142 offset:32768
	ds_read_b128 v[150:153], v142 offset:33792
	ds_read_b128 v[154:157], v142 offset:34816
	ds_read_b128 v[158:161], v142 offset:35840
	ds_read_b128 v[162:165], v142 offset:49152
	ds_read_b128 v[166:169], v142 offset:50176
	ds_read_b128 v[170:173], v142 offset:51200
	ds_read_b128 v[178:181], v142 offset:52224
	s_add_u32 s42, s54, 0x80000
	s_addc_u32 s43, s55, 0
	s_mov_b32 m0, s60
	v_lshl_add_u64 v[232:233], s[42:43], 0, v[136:137]
	ds_read_b128 v[182:185], v145 offset:32768
	ds_read_b128 v[186:189], v145 offset:33792
	ds_read_b128 v[190:193], v145 offset:34816
	ds_read_b128 v[194:197], v145 offset:35840
	ds_read_b128 v[198:201], v145 offset:36864
	ds_read_b128 v[202:205], v145 offset:37888
	ds_read_b128 v[206:209], v145 offset:38912
	ds_read_b128 v[226:229], v145 offset:39936
	global_load_lds_dwordx4 v[232:233], off
	v_lshl_add_u64 v[232:233], s[42:43], 0, v[134:135]
	s_mov_b32 m0, s61
	s_nop 0
	global_load_lds_dwordx4 v[232:233], off
	s_waitcnt vmcnt(8)
	s_waitcnt lgkmcnt(0)
	s_barrier
	s_setprio 1
	s_waitcnt lgkmcnt(0)
	v_mfma_f32_16x16x32_bf16 v[128:131], v[146:149], v[182:185], v[128:131]
	v_mfma_f32_16x16x32_bf16 v[124:127], v[154:157], v[182:185], v[124:127]
	v_mfma_f32_16x16x32_bf16 v[120:123], v[146:149], v[190:193], v[120:123]
	v_mfma_f32_16x16x32_bf16 v[116:119], v[154:157], v[190:193], v[116:119]
	v_mfma_f32_16x16x32_bf16 v[104:107], v[146:149], v[198:201], v[104:107]
	v_mfma_f32_16x16x32_bf16 v[100:103], v[154:157], v[198:201], v[100:103]
	v_mfma_f32_16x16x32_bf16 v[88:91], v[146:149], v[206:209], v[88:91]
	v_mfma_f32_16x16x32_bf16 v[84:87], v[154:157], v[206:209], v[84:87]
	v_mfma_f32_16x16x32_bf16 v[128:131], v[150:153], v[186:189], v[128:131]
	v_mfma_f32_16x16x32_bf16 v[124:127], v[158:161], v[186:189], v[124:127]
	v_mfma_f32_16x16x32_bf16 v[120:123], v[150:153], v[194:197], v[120:123]
	v_mfma_f32_16x16x32_bf16 v[116:119], v[158:161], v[194:197], v[116:119]
	v_mfma_f32_16x16x32_bf16 v[104:107], v[150:153], v[202:205], v[104:107]
	v_mfma_f32_16x16x32_bf16 v[100:103], v[158:161], v[202:205], v[100:103]
	v_mfma_f32_16x16x32_bf16 v[88:91], v[150:153], v[226:229], v[88:91]
	v_mfma_f32_16x16x32_bf16 v[84:87], v[158:161], v[226:229], v[84:87]
	s_setprio 0
	s_setprio 1
	v_mfma_f32_16x16x32_bf16 v[112:115], v[162:165], v[182:185], v[112:115]
	v_mfma_f32_16x16x32_bf16 v[108:111], v[170:173], v[182:185], v[108:111]
	v_mfma_f32_16x16x32_bf16 v[96:99], v[162:165], v[190:193], v[96:99]
	v_mfma_f32_16x16x32_bf16 v[92:95], v[170:173], v[190:193], v[92:95]
	v_mfma_f32_16x16x32_bf16 v[80:83], v[162:165], v[198:201], v[80:83]
	v_mfma_f32_16x16x32_bf16 v[76:79], v[170:173], v[198:201], v[76:79]
	v_mfma_f32_16x16x32_bf16 v[72:75], v[162:165], v[206:209], v[72:75]
	v_mfma_f32_16x16x32_bf16 v[68:71], v[170:173], v[206:209], v[68:71]
	v_mfma_f32_16x16x32_bf16 v[112:115], v[166:169], v[186:189], v[112:115]
	v_mfma_f32_16x16x32_bf16 v[108:111], v[178:181], v[186:189], v[108:111]
	v_mfma_f32_16x16x32_bf16 v[96:99], v[166:169], v[194:197], v[96:99]
	v_mfma_f32_16x16x32_bf16 v[92:95], v[178:181], v[194:197], v[92:95]
	v_mfma_f32_16x16x32_bf16 v[80:83], v[166:169], v[202:205], v[80:83]
	v_mfma_f32_16x16x32_bf16 v[76:79], v[178:181], v[202:205], v[76:79]
	v_mfma_f32_16x16x32_bf16 v[72:75], v[166:169], v[226:229], v[72:75]
	v_mfma_f32_16x16x32_bf16 v[68:71], v[178:181], v[226:229], v[68:71]
	s_setprio 0
	s_barrier
	s_add_i32 s42, s70, s57
	v_lshl_add_u64 v[174:175], v[174:175], 0, s[6:7]
	s_mov_b32 m0, s42
	ds_read_b128 v[182:185], v145 offset:49152
	ds_read_b128 v[186:189], v145 offset:50176
	ds_read_b128 v[190:193], v145 offset:51200
	ds_read_b128 v[194:197], v145 offset:52224
	ds_read_b128 v[198:201], v145 offset:53248
	ds_read_b128 v[202:205], v145 offset:54272
	ds_read_b128 v[206:209], v145 offset:55296
	ds_read_b128 v[226:229], v145 offset:56320
	global_load_lds_dwordx4 v[174:175], off
	s_add_i32 m0, s42, 0x2000
	s_add_u32 s42, s52, 0x80080
	v_lshl_add_u64 v[174:175], v[210:211], 0, s[6:7]
	s_addc_u32 s43, s53, 0
	s_add_i32 s52, s71, s57
	global_load_lds_dwordx4 v[174:175], off
	v_lshl_add_u64 v[174:175], s[42:43], 0, v[2:3]
	s_mov_b32 m0, s52
	s_nop 0
	global_load_lds_dwordx4 v[174:175], off
	v_lshl_add_u64 v[174:175], s[42:43], 0, v[132:133]
	s_add_i32 m0, s52, 0x2000
	s_nop 0
	global_load_lds_dwordx4 v[174:175], off
	v_lshl_add_u64 v[174:175], v[214:215], 0, s[6:7]
	s_mov_b32 m0, s62
	s_nop 0
	global_load_lds_dwordx4 v[174:175], off
	v_lshl_add_u64 v[174:175], v[230:231], 0, s[6:7]
	s_mov_b32 m0, s63
	s_nop 0
	global_load_lds_dwordx4 v[174:175], off
	s_waitcnt vmcnt(8)
	s_waitcnt lgkmcnt(0)
	s_barrier
	s_setprio 1
	s_waitcnt lgkmcnt(0)
	v_mfma_f32_16x16x32_bf16 v[64:67], v[146:149], v[182:185], v[64:67]
	v_mfma_f32_16x16x32_bf16 v[60:63], v[154:157], v[182:185], v[60:63]
	v_mfma_f32_16x16x32_bf16 v[56:59], v[146:149], v[190:193], v[56:59]
	v_mfma_f32_16x16x32_bf16 v[52:55], v[154:157], v[190:193], v[52:55]
	v_mfma_f32_16x16x32_bf16 v[40:43], v[146:149], v[198:201], v[40:43]
	v_mfma_f32_16x16x32_bf16 v[36:39], v[154:157], v[198:201], v[36:39]
	v_mfma_f32_16x16x32_bf16 v[24:27], v[146:149], v[206:209], v[24:27]
	v_mfma_f32_16x16x32_bf16 v[20:23], v[154:157], v[206:209], v[20:23]
	v_mfma_f32_16x16x32_bf16 v[64:67], v[150:153], v[186:189], v[64:67]
	v_mfma_f32_16x16x32_bf16 v[60:63], v[158:161], v[186:189], v[60:63]
	v_mfma_f32_16x16x32_bf16 v[56:59], v[150:153], v[194:197], v[56:59]
	v_mfma_f32_16x16x32_bf16 v[52:55], v[158:161], v[194:197], v[52:55]
	v_mfma_f32_16x16x32_bf16 v[40:43], v[150:153], v[202:205], v[40:43]
	v_mfma_f32_16x16x32_bf16 v[36:39], v[158:161], v[202:205], v[36:39]
	v_mfma_f32_16x16x32_bf16 v[24:27], v[150:153], v[226:229], v[24:27]
	v_mfma_f32_16x16x32_bf16 v[20:23], v[158:161], v[226:229], v[20:23]
	s_setprio 0
	s_setprio 1
	v_mfma_f32_16x16x32_bf16 v[48:51], v[162:165], v[182:185], v[48:51]
	v_mfma_f32_16x16x32_bf16 v[44:47], v[170:173], v[182:185], v[44:47]
	v_mfma_f32_16x16x32_bf16 v[32:35], v[162:165], v[190:193], v[32:35]
	v_mfma_f32_16x16x32_bf16 v[28:31], v[170:173], v[190:193], v[28:31]
	v_mfma_f32_16x16x32_bf16 v[16:19], v[162:165], v[198:201], v[16:19]
	v_mfma_f32_16x16x32_bf16 v[12:15], v[170:173], v[198:201], v[12:15]
	v_mfma_f32_16x16x32_bf16 v[8:11], v[162:165], v[206:209], v[8:11]
	v_mfma_f32_16x16x32_bf16 v[4:7], v[170:173], v[206:209], v[4:7]
	v_mfma_f32_16x16x32_bf16 v[48:51], v[166:169], v[186:189], v[48:51]
	v_mfma_f32_16x16x32_bf16 v[44:47], v[178:181], v[186:189], v[44:47]
	v_mfma_f32_16x16x32_bf16 v[32:35], v[166:169], v[194:197], v[32:35]
	v_mfma_f32_16x16x32_bf16 v[28:31], v[178:181], v[194:197], v[28:31]
	v_mfma_f32_16x16x32_bf16 v[16:19], v[166:169], v[202:205], v[16:19]
	v_mfma_f32_16x16x32_bf16 v[12:15], v[178:181], v[202:205], v[12:15]
	v_mfma_f32_16x16x32_bf16 v[8:11], v[166:169], v[226:229], v[8:11]
	v_mfma_f32_16x16x32_bf16 v[4:7], v[178:181], v[226:229], v[4:7]
	s_setprio 0
	s_add_i32 s69, s69, 2
	s_add_u32 s48, s48, 0x100
	s_addc_u32 s49, s49, 0
	s_add_u32 s67, s67, 0x100
	s_addc_u32 s68, s68, 0
	s_cmp_gt_u32 s69, 29
	s_cbranch_scc1 .Lmy_kx_1427
	s_add_u32 s42, s48, 0xfff80080
	s_addc_u32 s43, s49, -1
	s_add_i32 s70, 0, 0x10000
	s_cmp_eq_u32 s69, 28
	s_cselect_b32 s55, s10, s43
	s_cselect_b32 s54, s11, s42
	s_cselect_b32 s53, s39, s68
	s_cselect_b32 s52, s41, s67
	s_add_i32 s71, 0, 0x14000
	s_cmp_gt_u32 s69, 29

.Lmy_kl_1772:
	ds_read_b128 v[20:23], v190
	ds_read_b128 v[28:31], v190 offset:2048
	ds_read_b128 v[24:27], v190 offset:1024
	ds_read_b128 v[32:35], v190 offset:3072
	ds_read_b128 v[4:7], v190 offset:16384
	ds_read_b128 v[12:15], v190 offset:18432
	ds_read_b128 v[8:11], v190 offset:17408
	ds_read_b128 v[16:19], v190 offset:19456
	v_lshl_add_u64 v[174:175], s[50:51], 0, v[170:171]
	s_add_i32 m0, s47, 0xc000
	ds_read_b128 v[178:181], v193
	ds_read_b128 v[196:199], v193 offset:2048
	ds_read_b128 v[182:185], v194
	ds_read_b128 v[200:203], v194 offset:2048
	ds_read_b128 v[204:207], v193 offset:4096
	ds_read_b128 v[226:229], v193 offset:6144
	ds_read_b128 v[208:211], v194 offset:4096
	ds_read_b128 v[230:233], v194 offset:6144
	global_load_lds_dwordx4 v[174:175], off
	v_lshl_add_u64 v[174:175], s[50:51], 0, v[172:173]
	s_add_i32 m0, s47, 0xe000
	s_nop 0
	global_load_lds_dwordx4 v[174:175], off
	s_waitcnt vmcnt(8)
	s_waitcnt lgkmcnt(0)
	s_barrier
	s_setprio 1
	s_waitcnt lgkmcnt(0)
	v_mfma_scale_f32_16x16x128_f8f6f4 v[160:163], v[20:27], v[178:185], v[160:163], v219, v220 op_sel_hi:[0,0,0]
	v_mfma_scale_f32_16x16x128_f8f6f4 v[152:155], v[28:35], v[178:185], v[152:155], v219, v220 op_sel_hi:[0,0,0]
	v_mfma_scale_f32_16x16x128_f8f6f4 v[144:147], v[20:27], v[196:203], v[144:147], v219, v220 op_sel_hi:[0,0,0]
	v_mfma_scale_f32_16x16x128_f8f6f4 v[136:139], v[28:35], v[196:203], v[136:139], v219, v220 op_sel_hi:[0,0,0]
	v_mfma_scale_f32_16x16x128_f8f6f4 v[128:131], v[20:27], v[204:211], v[128:131], v219, v220 op_sel_hi:[0,0,0]
	v_mfma_scale_f32_16x16x128_f8f6f4 v[120:123], v[28:35], v[204:211], v[120:123], v219, v220 op_sel_hi:[0,0,0]
	v_mfma_scale_f32_16x16x128_f8f6f4 v[112:115], v[20:27], v[226:233], v[112:115], v219, v220 op_sel_hi:[0,0,0]
	v_mfma_scale_f32_16x16x128_f8f6f4 v[104:107], v[28:35], v[226:233], v[104:107], v219, v220 op_sel_hi:[0,0,0]
	s_setprio 0
	s_setprio 1
	v_mfma_scale_f32_16x16x128_f8f6f4 v[156:159], v[4:11], v[178:185], v[156:159], v219, v220 op_sel_hi:[0,0,0]
	v_mfma_scale_f32_16x16x128_f8f6f4 v[148:151], v[12:19], v[178:185], v[148:151], v219, v220 op_sel_hi:[0,0,0]
	v_mfma_scale_f32_16x16x128_f8f6f4 v[140:143], v[4:11], v[196:203], v[140:143], v219, v220 op_sel_hi:[0,0,0]
	v_mfma_scale_f32_16x16x128_f8f6f4 v[132:135], v[12:19], v[196:203], v[132:135], v219, v220 op_sel_hi:[0,0,0]
	v_mfma_scale_f32_16x16x128_f8f6f4 v[124:127], v[4:11], v[204:211], v[124:127], v219, v220 op_sel_hi:[0,0,0]
	v_mfma_scale_f32_16x16x128_f8f6f4 v[116:119], v[12:19], v[204:211], v[116:119], v219, v220 op_sel_hi:[0,0,0]
	v_mfma_scale_f32_16x16x128_f8f6f4 v[108:111], v[4:11], v[226:233], v[108:111], v219, v220 op_sel_hi:[0,0,0]
	v_mfma_scale_f32_16x16x128_f8f6f4 v[100:103], v[12:19], v[226:233], v[100:103], v219, v220 op_sel_hi:[0,0,0]
	s_setprio 0
	s_barrier
	s_add_i32 s42, s42, s57
	v_lshl_add_u64 v[182:183], s[52:53], 0, v[2:3]
	s_mov_b32 m0, s42
	ds_read_b128 v[196:199], v193 offset:16384
	ds_read_b128 v[204:207], v193 offset:18432
	ds_read_b128 v[200:203], v194 offset:16384
	ds_read_b128 v[208:211], v194 offset:18432
	ds_read_b128 v[226:229], v193 offset:20480
	ds_read_b128 v[234:237], v193 offset:22528
	ds_read_b128 v[230:233], v194 offset:20480
	ds_read_b128 v[238:241], v194 offset:22528
	global_load_lds_dwordx4 v[182:183], off
	s_add_i32 m0, s42, 0x2000
	s_add_u32 s70, s52, 0x40000
	v_lshl_add_u64 v[184:185], s[52:53], 0, v[164:165]
	s_addc_u32 s71, s53, 0
	s_add_i32 s42, s43, s57
	global_load_lds_dwordx4 v[184:185], off
	v_lshl_add_u64 v[174:175], s[70:71], 0, v[2:3]
	s_mov_b32 m0, s42
	v_lshl_add_u64 v[186:187], s[54:55], 0, v[168:169]
	global_load_lds_dwordx4 v[174:175], off
	v_lshl_add_u64 v[174:175], s[70:71], 0, v[164:165]
	s_add_i32 m0, s42, 0x2000
	v_lshl_add_u64 v[188:189], s[54:55], 0, v[166:167]
	global_load_lds_dwordx4 v[174:175], off
	s_mov_b32 m0, s47
	s_nop 0
	global_load_lds_dwordx4 v[186:187], off
	s_mov_b32 m0, s49
	s_nop 0
	global_load_lds_dwordx4 v[188:189], off
	s_waitcnt vmcnt(8)
	s_waitcnt lgkmcnt(0)
	s_barrier
	s_setprio 1
	s_waitcnt lgkmcnt(0)
	v_mfma_scale_f32_16x16x128_f8f6f4 v[96:99], v[20:27], v[196:203], v[96:99], v219, v220 op_sel_hi:[0,0,0]
	v_mfma_scale_f32_16x16x128_f8f6f4 v[88:91], v[28:35], v[196:203], v[88:91], v219, v220 op_sel_hi:[0,0,0]
	v_mfma_scale_f32_16x16x128_f8f6f4 v[80:83], v[20:27], v[204:211], v[80:83], v219, v220 op_sel_hi:[0,0,0]
	v_mfma_scale_f32_16x16x128_f8f6f4 v[72:75], v[28:35], v[204:211], v[72:75], v219, v220 op_sel_hi:[0,0,0]
	v_mfma_scale_f32_16x16x128_f8f6f4 v[64:67], v[20:27], v[226:233], v[64:67], v219, v220 op_sel_hi:[0,0,0]
	v_mfma_scale_f32_16x16x128_f8f6f4 v[56:59], v[28:35], v[226:233], v[56:59], v219, v220 op_sel_hi:[0,0,0]
	v_mfma_scale_f32_16x16x128_f8f6f4 v[48:51], v[20:27], v[234:241], v[48:51], v219, v220 op_sel_hi:[0,0,0]
	v_mfma_scale_f32_16x16x128_f8f6f4 v[40:43], v[28:35], v[234:241], v[40:43], v219, v220 op_sel_hi:[0,0,0]
	s_setprio 0
	s_setprio 1
	v_mfma_scale_f32_16x16x128_f8f6f4 v[92:95], v[4:11], v[196:203], v[92:95], v219, v220 op_sel_hi:[0,0,0]
	v_mfma_scale_f32_16x16x128_f8f6f4 v[84:87], v[12:19], v[196:203], v[84:87], v219, v220 op_sel_hi:[0,0,0]
	v_mfma_scale_f32_16x16x128_f8f6f4 v[76:79], v[4:11], v[204:211], v[76:79], v219, v220 op_sel_hi:[0,0,0]
	v_mfma_scale_f32_16x16x128_f8f6f4 v[68:71], v[12:19], v[204:211], v[68:71], v219, v220 op_sel_hi:[0,0,0]
	v_mfma_scale_f32_16x16x128_f8f6f4 v[60:63], v[4:11], v[226:233], v[60:63], v219, v220 op_sel_hi:[0,0,0]
	v_mfma_scale_f32_16x16x128_f8f6f4 v[52:55], v[12:19], v[226:233], v[52:55], v219, v220 op_sel_hi:[0,0,0]
	v_mfma_scale_f32_16x16x128_f8f6f4 v[44:47], v[4:11], v[234:241], v[44:47], v219, v220 op_sel_hi:[0,0,0]
	v_mfma_scale_f32_16x16x128_f8f6f4 v[36:39], v[12:19], v[234:241], v[36:39], v219, v220 op_sel_hi:[0,0,0]
	s_setprio 0
	s_barrier
	s_add_i32 s69, 0, 0x18000
	s_add_i32 s70, 0, 0x1c000
	ds_read_b128 v[4:7], v190 offset:32768
	ds_read_b128 v[12:15], v190 offset:34816
	ds_read_b128 v[8:11], v190 offset:33792
	ds_read_b128 v[16:19], v190 offset:35840
	ds_read_b128 v[20:23], v190 offset:49152
	ds_read_b128 v[28:31], v190 offset:51200
	ds_read_b128 v[24:27], v190 offset:50176
	ds_read_b128 v[32:35], v190 offset:52224
	s_add_u32 s42, s54, 0x40000
	s_addc_u32 s43, s55, 0
	s_mov_b32 m0, s61
	v_lshl_add_u64 v[174:175], s[42:43], 0, v[168:169]
	ds_read_b128 v[196:199], v193 offset:32768
	ds_read_b128 v[204:207], v193 offset:34816
	ds_read_b128 v[200:203], v194 offset:32768
	ds_read_b128 v[208:211], v194 offset:34816
	ds_read_b128 v[226:229], v193 offset:36864
	ds_read_b128 v[234:237], v193 offset:38912
	ds_read_b128 v[230:233], v194 offset:36864
	ds_read_b128 v[238:241], v194 offset:38912
	global_load_lds_dwordx4 v[174:175], off
	v_lshl_add_u64 v[174:175], s[42:43], 0, v[166:167]
	s_mov_b32 m0, s62
	s_nop 0
	global_load_lds_dwordx4 v[174:175], off
	s_waitcnt vmcnt(8)
	s_waitcnt lgkmcnt(0)
	s_barrier
	s_setprio 1
	s_waitcnt lgkmcnt(0)
	v_mfma_scale_f32_16x16x128_f8f6f4 v[160:163], v[4:11], v[196:203], v[160:163], v219, v220 op_sel_hi:[0,0,0]
	v_mfma_scale_f32_16x16x128_f8f6f4 v[152:155], v[12:19], v[196:203], v[152:155], v219, v220 op_sel_hi:[0,0,0]
	v_mfma_scale_f32_16x16x128_f8f6f4 v[144:147], v[4:11], v[204:211], v[144:147], v219, v220 op_sel_hi:[0,0,0]
	v_mfma_scale_f32_16x16x128_f8f6f4 v[136:139], v[12:19], v[204:211], v[136:139], v219, v220 op_sel_hi:[0,0,0]
	v_mfma_scale_f32_16x16x128_f8f6f4 v[128:131], v[4:11], v[226:233], v[128:131], v219, v220 op_sel_hi:[0,0,0]
	v_mfma_scale_f32_16x16x128_f8f6f4 v[120:123], v[12:19], v[226:233], v[120:123], v219, v220 op_sel_hi:[0,0,0]
	v_mfma_scale_f32_16x16x128_f8f6f4 v[112:115], v[4:11], v[234:241], v[112:115], v219, v220 op_sel_hi:[0,0,0]
	v_mfma_scale_f32_16x16x128_f8f6f4 v[104:107], v[12:19], v[234:241], v[104:107], v219, v220 op_sel_hi:[0,0,0]
	s_setprio 0
	s_setprio 1
	v_mfma_scale_f32_16x16x128_f8f6f4 v[156:159], v[20:27], v[196:203], v[156:159], v219, v220 op_sel_hi:[0,0,0]
	v_mfma_scale_f32_16x16x128_f8f6f4 v[148:151], v[28:35], v[196:203], v[148:151], v219, v220 op_sel_hi:[0,0,0]
	v_mfma_scale_f32_16x16x128_f8f6f4 v[140:143], v[20:27], v[204:211], v[140:143], v219, v220 op_sel_hi:[0,0,0]
	v_mfma_scale_f32_16x16x128_f8f6f4 v[132:135], v[28:35], v[204:211], v[132:135], v219, v220 op_sel_hi:[0,0,0]
	v_mfma_scale_f32_16x16x128_f8f6f4 v[124:127], v[20:27], v[226:233], v[124:127], v219, v220 op_sel_hi:[0,0,0]
	v_mfma_scale_f32_16x16x128_f8f6f4 v[116:119], v[28:35], v[226:233], v[116:119], v219, v220 op_sel_hi:[0,0,0]
	v_mfma_scale_f32_16x16x128_f8f6f4 v[108:111], v[20:27], v[234:241], v[108:111], v219, v220 op_sel_hi:[0,0,0]
	v_mfma_scale_f32_16x16x128_f8f6f4 v[100:103], v[28:35], v[234:241], v[100:103], v219, v220 op_sel_hi:[0,0,0]
	s_setprio 0
	s_barrier
	s_add_i32 s42, s69, s57
	v_lshl_add_u64 v[174:175], v[182:183], 0, s[6:7]
	s_mov_b32 m0, s42
	ds_read_b128 v[196:199], v193 offset:49152
	ds_read_b128 v[204:207], v193 offset:51200
	ds_read_b128 v[200:203], v194 offset:49152
	ds_read_b128 v[208:211], v194 offset:51200
	ds_read_b128 v[226:229], v193 offset:53248
	ds_read_b128 v[234:237], v193 offset:55296
	ds_read_b128 v[230:233], v194 offset:53248
	ds_read_b128 v[238:241], v194 offset:55296
	global_load_lds_dwordx4 v[174:175], off
	s_add_i32 m0, s42, 0x2000
	s_add_u32 s42, s52, 0x40080
	v_lshl_add_u64 v[174:175], v[184:185], 0, s[6:7]
	s_addc_u32 s43, s53, 0
	s_add_i32 s52, s70, s57
	global_load_lds_dwordx4 v[174:175], off
	v_lshl_add_u64 v[174:175], s[42:43], 0, v[2:3]
	s_mov_b32 m0, s52
	s_nop 0
	global_load_lds_dwordx4 v[174:175], off
	v_lshl_add_u64 v[174:175], s[42:43], 0, v[164:165]
	s_add_i32 m0, s52, 0x2000
	s_nop 0
	global_load_lds_dwordx4 v[174:175], off
	v_lshl_add_u64 v[174:175], v[186:187], 0, s[6:7]
	s_mov_b32 m0, s63
	s_nop 0
	global_load_lds_dwordx4 v[174:175], off
	v_lshl_add_u64 v[174:175], v[188:189], 0, s[6:7]
	s_mov_b32 m0, s64
	s_nop 0
	global_load_lds_dwordx4 v[174:175], off
	s_waitcnt vmcnt(8)
	s_waitcnt lgkmcnt(0)
	s_barrier
	s_setprio 1
	s_waitcnt lgkmcnt(0)
	v_mfma_scale_f32_16x16x128_f8f6f4 v[96:99], v[4:11], v[196:203], v[96:99], v219, v220 op_sel_hi:[0,0,0]
	v_mfma_scale_f32_16x16x128_f8f6f4 v[88:91], v[12:19], v[196:203], v[88:91], v219, v220 op_sel_hi:[0,0,0]
	v_mfma_scale_f32_16x16x128_f8f6f4 v[80:83], v[4:11], v[204:211], v[80:83], v219, v220 op_sel_hi:[0,0,0]
	v_mfma_scale_f32_16x16x128_f8f6f4 v[72:75], v[12:19], v[204:211], v[72:75], v219, v220 op_sel_hi:[0,0,0]
	v_mfma_scale_f32_16x16x128_f8f6f4 v[64:67], v[4:11], v[226:233], v[64:67], v219, v220 op_sel_hi:[0,0,0]
	v_mfma_scale_f32_16x16x128_f8f6f4 v[56:59], v[12:19], v[226:233], v[56:59], v219, v220 op_sel_hi:[0,0,0]
	v_mfma_scale_f32_16x16x128_f8f6f4 v[48:51], v[4:11], v[234:241], v[48:51], v219, v220 op_sel_hi:[0,0,0]
	v_mfma_scale_f32_16x16x128_f8f6f4 v[40:43], v[12:19], v[234:241], v[40:43], v219, v220 op_sel_hi:[0,0,0]
	s_setprio 0
	s_setprio 1
	v_mfma_scale_f32_16x16x128_f8f6f4 v[92:95], v[20:27], v[196:203], v[92:95], v219, v220 op_sel_hi:[0,0,0]
	v_mfma_scale_f32_16x16x128_f8f6f4 v[84:87], v[28:35], v[196:203], v[84:87], v219, v220 op_sel_hi:[0,0,0]
	v_mfma_scale_f32_16x16x128_f8f6f4 v[76:79], v[20:27], v[204:211], v[76:79], v219, v220 op_sel_hi:[0,0,0]
	v_mfma_scale_f32_16x16x128_f8f6f4 v[68:71], v[28:35], v[204:211], v[68:71], v219, v220 op_sel_hi:[0,0,0]
	v_mfma_scale_f32_16x16x128_f8f6f4 v[60:63], v[20:27], v[226:233], v[60:63], v219, v220 op_sel_hi:[0,0,0]
	v_mfma_scale_f32_16x16x128_f8f6f4 v[52:55], v[28:35], v[226:233], v[52:55], v219, v220 op_sel_hi:[0,0,0]
	v_mfma_scale_f32_16x16x128_f8f6f4 v[44:47], v[20:27], v[234:241], v[44:47], v219, v220 op_sel_hi:[0,0,0]
	v_mfma_scale_f32_16x16x128_f8f6f4 v[36:39], v[28:35], v[234:241], v[36:39], v219, v220 op_sel_hi:[0,0,0]
	s_setprio 0
	s_add_i32 s68, s68, 2
	s_add_u32 s50, s50, 0x100
	s_addc_u32 s51, s51, 0
	s_add_u32 s66, s66, 0x100
	s_addc_u32 s67, s67, 0
	s_cmp_gt_u32 s68, 13
	s_cbranch_scc1 .Lmy_kx_1772
	s_add_u32 s43, s50, 0xfffc0080
	s_addc_u32 s52, s51, -1
	s_add_i32 s42, 0, 0x10000
	s_cmp_eq_u32 s68, 12
	s_cselect_b32 s55, s10, s52
	s_cselect_b32 s54, s11, s43
	s_cselect_b32 s53, s37, s67
	s_cselect_b32 s52, s39, s66
	s_add_i32 s43, 0, 0x14000
	s_cmp_gt_u32 s68, 13
.Lmy_kx_1772:
	s_barrier
	s_cbranch_scc0 .Lmy_kl_1772
	s_nop 15
	s_nop 15
	s_and_b64 vcc, exec, s[14:15]
	s_cbranch_vccz .LBB0_1775
	s_barrier

.Lmy_kl_1812:
	ds_read_b128 v[20:23], v190
	ds_read_b128 v[28:31], v190 offset:2048
	ds_read_b128 v[24:27], v190 offset:1024
	ds_read_b128 v[32:35], v190 offset:3072
	ds_read_b128 v[4:7], v190 offset:16384
	ds_read_b128 v[12:15], v190 offset:18432
	ds_read_b128 v[8:11], v190 offset:17408
	ds_read_b128 v[16:19], v190 offset:19456
	v_lshl_add_u64 v[174:175], s[52:53], 0, v[170:171]
	s_add_i32 m0, s49, 0xc000
	ds_read_b128 v[178:181], v193
	ds_read_b128 v[196:199], v193 offset:2048
	ds_read_b128 v[182:185], v194
	ds_read_b128 v[200:203], v194 offset:2048
	ds_read_b128 v[204:207], v193 offset:4096
	ds_read_b128 v[226:229], v193 offset:6144
	ds_read_b128 v[208:211], v194 offset:4096
	ds_read_b128 v[230:233], v194 offset:6144
	global_load_lds_dwordx4 v[174:175], off
	v_lshl_add_u64 v[174:175], s[52:53], 0, v[172:173]
	s_add_i32 m0, s49, 0xe000
	s_nop 0
	global_load_lds_dwordx4 v[174:175], off
	s_waitcnt vmcnt(8)
	s_waitcnt lgkmcnt(0)
	s_barrier
	s_setprio 1
	s_waitcnt lgkmcnt(0)
	v_mfma_scale_f32_16x16x128_f8f6f4 v[160:163], v[20:27], v[178:185], v[160:163], v219, v220 op_sel_hi:[0,0,0]
	v_mfma_scale_f32_16x16x128_f8f6f4 v[152:155], v[28:35], v[178:185], v[152:155], v219, v220 op_sel_hi:[0,0,0]
	v_mfma_scale_f32_16x16x128_f8f6f4 v[144:147], v[20:27], v[196:203], v[144:147], v219, v220 op_sel_hi:[0,0,0]
	v_mfma_scale_f32_16x16x128_f8f6f4 v[136:139], v[28:35], v[196:203], v[136:139], v219, v220 op_sel_hi:[0,0,0]
	v_mfma_scale_f32_16x16x128_f8f6f4 v[128:131], v[20:27], v[204:211], v[128:131], v219, v220 op_sel_hi:[0,0,0]
	v_mfma_scale_f32_16x16x128_f8f6f4 v[120:123], v[28:35], v[204:211], v[120:123], v219, v220 op_sel_hi:[0,0,0]
	v_mfma_scale_f32_16x16x128_f8f6f4 v[112:115], v[20:27], v[226:233], v[112:115], v219, v220 op_sel_hi:[0,0,0]
	v_mfma_scale_f32_16x16x128_f8f6f4 v[104:107], v[28:35], v[226:233], v[104:107], v219, v220 op_sel_hi:[0,0,0]
	s_setprio 0
	s_setprio 1
	v_mfma_scale_f32_16x16x128_f8f6f4 v[156:159], v[4:11], v[178:185], v[156:159], v219, v220 op_sel_hi:[0,0,0]
	v_mfma_scale_f32_16x16x128_f8f6f4 v[148:151], v[12:19], v[178:185], v[148:151], v219, v220 op_sel_hi:[0,0,0]
	v_mfma_scale_f32_16x16x128_f8f6f4 v[140:143], v[4:11], v[196:203], v[140:143], v219, v220 op_sel_hi:[0,0,0]
	v_mfma_scale_f32_16x16x128_f8f6f4 v[132:135], v[12:19], v[196:203], v[132:135], v219, v220 op_sel_hi:[0,0,0]
	v_mfma_scale_f32_16x16x128_f8f6f4 v[124:127], v[4:11], v[204:211], v[124:127], v219, v220 op_sel_hi:[0,0,0]
	v_mfma_scale_f32_16x16x128_f8f6f4 v[116:119], v[12:19], v[204:211], v[116:119], v219, v220 op_sel_hi:[0,0,0]
	v_mfma_scale_f32_16x16x128_f8f6f4 v[108:111], v[4:11], v[226:233], v[108:111], v219, v220 op_sel_hi:[0,0,0]
	v_mfma_scale_f32_16x16x128_f8f6f4 v[100:103], v[12:19], v[226:233], v[100:103], v219, v220 op_sel_hi:[0,0,0]
	s_setprio 0
	s_barrier
	s_add_i32 s42, s42, s69
	v_lshl_add_u64 v[182:183], s[54:55], 0, v[2:3]
	s_mov_b32 m0, s42
	ds_read_b128 v[196:199], v193 offset:16384
	ds_read_b128 v[204:207], v193 offset:18432
	ds_read_b128 v[200:203], v194 offset:16384
	ds_read_b128 v[208:211], v194 offset:18432
	ds_read_b128 v[226:229], v193 offset:20480
	ds_read_b128 v[234:237], v193 offset:22528
	ds_read_b128 v[230:233], v194 offset:20480
	ds_read_b128 v[238:241], v194 offset:22528
	global_load_lds_dwordx4 v[182:183], off
	s_add_i32 m0, s42, 0x2000
	s_add_u32 s80, s54, 0x40000
	v_lshl_add_u64 v[184:185], s[54:55], 0, v[168:169]
	s_addc_u32 s81, s55, 0
	s_add_i32 s42, s43, s69
	global_load_lds_dwordx4 v[184:185], off
	v_lshl_add_u64 v[174:175], s[80:81], 0, v[2:3]
	s_mov_b32 m0, s42
	v_lshl_add_u64 v[186:187], s[56:57], 0, v[164:165]
	global_load_lds_dwordx4 v[174:175], off
	v_lshl_add_u64 v[174:175], s[80:81], 0, v[168:169]
	s_add_i32 m0, s42, 0x2000
	v_lshl_add_u64 v[188:189], s[56:57], 0, v[166:167]
	global_load_lds_dwordx4 v[174:175], off
	s_mov_b32 m0, s49
	s_nop 0
	global_load_lds_dwordx4 v[186:187], off
	s_mov_b32 m0, s51
	s_nop 0
	global_load_lds_dwordx4 v[188:189], off
	s_waitcnt vmcnt(8)
	s_waitcnt lgkmcnt(0)
	s_barrier
	s_setprio 1
	s_waitcnt lgkmcnt(0)
	v_mfma_scale_f32_16x16x128_f8f6f4 v[96:99], v[20:27], v[196:203], v[96:99], v219, v220 op_sel_hi:[0,0,0]
	v_mfma_scale_f32_16x16x128_f8f6f4 v[88:91], v[28:35], v[196:203], v[88:91], v219, v220 op_sel_hi:[0,0,0]
	v_mfma_scale_f32_16x16x128_f8f6f4 v[80:83], v[20:27], v[204:211], v[80:83], v219, v220 op_sel_hi:[0,0,0]
	v_mfma_scale_f32_16x16x128_f8f6f4 v[72:75], v[28:35], v[204:211], v[72:75], v219, v220 op_sel_hi:[0,0,0]
	v_mfma_scale_f32_16x16x128_f8f6f4 v[64:67], v[20:27], v[226:233], v[64:67], v219, v220 op_sel_hi:[0,0,0]
	v_mfma_scale_f32_16x16x128_f8f6f4 v[56:59], v[28:35], v[226:233], v[56:59], v219, v220 op_sel_hi:[0,0,0]
	v_mfma_scale_f32_16x16x128_f8f6f4 v[48:51], v[20:27], v[234:241], v[48:51], v219, v220 op_sel_hi:[0,0,0]
	v_mfma_scale_f32_16x16x128_f8f6f4 v[40:43], v[28:35], v[234:241], v[40:43], v219, v220 op_sel_hi:[0,0,0]
	s_setprio 0
	s_setprio 1
	v_mfma_scale_f32_16x16x128_f8f6f4 v[92:95], v[4:11], v[196:203], v[92:95], v219, v220 op_sel_hi:[0,0,0]
	v_mfma_scale_f32_16x16x128_f8f6f4 v[84:87], v[12:19], v[196:203], v[84:87], v219, v220 op_sel_hi:[0,0,0]
	v_mfma_scale_f32_16x16x128_f8f6f4 v[76:79], v[4:11], v[204:211], v[76:79], v219, v220 op_sel_hi:[0,0,0]
	v_mfma_scale_f32_16x16x128_f8f6f4 v[68:71], v[12:19], v[204:211], v[68:71], v219, v220 op_sel_hi:[0,0,0]
	v_mfma_scale_f32_16x16x128_f8f6f4 v[60:63], v[4:11], v[226:233], v[60:63], v219, v220 op_sel_hi:[0,0,0]
	v_mfma_scale_f32_16x16x128_f8f6f4 v[52:55], v[12:19], v[226:233], v[52:55], v219, v220 op_sel_hi:[0,0,0]
	v_mfma_scale_f32_16x16x128_f8f6f4 v[44:47], v[4:11], v[234:241], v[44:47], v219, v220 op_sel_hi:[0,0,0]
	v_mfma_scale_f32_16x16x128_f8f6f4 v[36:39], v[12:19], v[234:241], v[36:39], v219, v220 op_sel_hi:[0,0,0]
	s_setprio 0
	s_barrier
	s_add_i32 s80, 0, 0x18000
	s_add_i32 s81, 0, 0x1c000
	ds_read_b128 v[4:7], v190 offset:32768
	ds_read_b128 v[12:15], v190 offset:34816
	ds_read_b128 v[8:11], v190 offset:33792
	ds_read_b128 v[16:19], v190 offset:35840
	ds_read_b128 v[20:23], v190 offset:49152
	ds_read_b128 v[28:31], v190 offset:51200
	ds_read_b128 v[24:27], v190 offset:50176
	ds_read_b128 v[32:35], v190 offset:52224
	s_add_u32 s42, s56, 0x40000
	s_addc_u32 s43, s57, 0
	s_mov_b32 m0, s72
	v_lshl_add_u64 v[174:175], s[42:43], 0, v[164:165]
	ds_read_b128 v[196:199], v193 offset:32768
	ds_read_b128 v[204:207], v193 offset:34816
	ds_read_b128 v[200:203], v194 offset:32768
	ds_read_b128 v[208:211], v194 offset:34816
	ds_read_b128 v[226:229], v193 offset:36864
	ds_read_b128 v[234:237], v193 offset:38912
	ds_read_b128 v[230:233], v194 offset:36864
	ds_read_b128 v[238:241], v194 offset:38912
	global_load_lds_dwordx4 v[174:175], off
	v_lshl_add_u64 v[174:175], s[42:43], 0, v[166:167]
	s_mov_b32 m0, s73
	s_nop 0
	global_load_lds_dwordx4 v[174:175], off
	s_waitcnt vmcnt(8)
	s_waitcnt lgkmcnt(0)
	s_barrier
	s_setprio 1
	s_waitcnt lgkmcnt(0)
	v_mfma_scale_f32_16x16x128_f8f6f4 v[160:163], v[4:11], v[196:203], v[160:163], v219, v220 op_sel_hi:[0,0,0]
	v_mfma_scale_f32_16x16x128_f8f6f4 v[152:155], v[12:19], v[196:203], v[152:155], v219, v220 op_sel_hi:[0,0,0]
	v_mfma_scale_f32_16x16x128_f8f6f4 v[144:147], v[4:11], v[204:211], v[144:147], v219, v220 op_sel_hi:[0,0,0]
	v_mfma_scale_f32_16x16x128_f8f6f4 v[136:139], v[12:19], v[204:211], v[136:139], v219, v220 op_sel_hi:[0,0,0]
	v_mfma_scale_f32_16x16x128_f8f6f4 v[128:131], v[4:11], v[226:233], v[128:131], v219, v220 op_sel_hi:[0,0,0]
	v_mfma_scale_f32_16x16x128_f8f6f4 v[120:123], v[12:19], v[226:233], v[120:123], v219, v220 op_sel_hi:[0,0,0]
	v_mfma_scale_f32_16x16x128_f8f6f4 v[112:115], v[4:11], v[234:241], v[112:115], v219, v220 op_sel_hi:[0,0,0]
	v_mfma_scale_f32_16x16x128_f8f6f4 v[104:107], v[12:19], v[234:241], v[104:107], v219, v220 op_sel_hi:[0,0,0]
	s_setprio 0
	s_setprio 1
	v_mfma_scale_f32_16x16x128_f8f6f4 v[156:159], v[20:27], v[196:203], v[156:159], v219, v220 op_sel_hi:[0,0,0]
	v_mfma_scale_f32_16x16x128_f8f6f4 v[148:151], v[28:35], v[196:203], v[148:151], v219, v220 op_sel_hi:[0,0,0]
	v_mfma_scale_f32_16x16x128_f8f6f4 v[140:143], v[20:27], v[204:211], v[140:143], v219, v220 op_sel_hi:[0,0,0]
	v_mfma_scale_f32_16x16x128_f8f6f4 v[132:135], v[28:35], v[204:211], v[132:135], v219, v220 op_sel_hi:[0,0,0]
	v_mfma_scale_f32_16x16x128_f8f6f4 v[124:127], v[20:27], v[226:233], v[124:127], v219, v220 op_sel_hi:[0,0,0]
	v_mfma_scale_f32_16x16x128_f8f6f4 v[116:119], v[28:35], v[226:233], v[116:119], v219, v220 op_sel_hi:[0,0,0]
	v_mfma_scale_f32_16x16x128_f8f6f4 v[108:111], v[20:27], v[234:241], v[108:111], v219, v220 op_sel_hi:[0,0,0]
	v_mfma_scale_f32_16x16x128_f8f6f4 v[100:103], v[28:35], v[234:241], v[100:103], v219, v220 op_sel_hi:[0,0,0]
	s_setprio 0
	s_barrier
	s_add_i32 s42, s80, s69
	v_lshl_add_u64 v[174:175], v[182:183], 0, s[6:7]
	s_mov_b32 m0, s42
	ds_read_b128 v[196:199], v193 offset:49152
	ds_read_b128 v[204:207], v193 offset:51200
	ds_read_b128 v[200:203], v194 offset:49152
	ds_read_b128 v[208:211], v194 offset:51200
	ds_read_b128 v[226:229], v193 offset:53248
	ds_read_b128 v[234:237], v193 offset:55296
	ds_read_b128 v[230:233], v194 offset:53248
	ds_read_b128 v[238:241], v194 offset:55296
	global_load_lds_dwordx4 v[174:175], off
	s_add_i32 m0, s42, 0x2000
	s_add_u32 s42, s54, 0x40080
	v_lshl_add_u64 v[174:175], v[184:185], 0, s[6:7]
	s_addc_u32 s43, s55, 0
	s_add_i32 s54, s81, s69
	global_load_lds_dwordx4 v[174:175], off
	v_lshl_add_u64 v[174:175], s[42:43], 0, v[2:3]
	s_mov_b32 m0, s54
	s_nop 0
	global_load_lds_dwordx4 v[174:175], off
	v_lshl_add_u64 v[174:175], s[42:43], 0, v[168:169]
	s_add_i32 m0, s54, 0x2000
	s_nop 0
	global_load_lds_dwordx4 v[174:175], off
	v_lshl_add_u64 v[174:175], v[186:187], 0, s[6:7]
	s_mov_b32 m0, s74
	s_nop 0
	global_load_lds_dwordx4 v[174:175], off
	v_lshl_add_u64 v[174:175], v[188:189], 0, s[6:7]
	s_mov_b32 m0, s75
	s_nop 0
	global_load_lds_dwordx4 v[174:175], off
	s_waitcnt vmcnt(8)
	s_waitcnt lgkmcnt(0)
	s_barrier
	s_setprio 1
	s_waitcnt lgkmcnt(0)
	v_mfma_scale_f32_16x16x128_f8f6f4 v[96:99], v[4:11], v[196:203], v[96:99], v219, v220 op_sel_hi:[0,0,0]
	v_mfma_scale_f32_16x16x128_f8f6f4 v[88:91], v[12:19], v[196:203], v[88:91], v219, v220 op_sel_hi:[0,0,0]
	v_mfma_scale_f32_16x16x128_f8f6f4 v[80:83], v[4:11], v[204:211], v[80:83], v219, v220 op_sel_hi:[0,0,0]
	v_mfma_scale_f32_16x16x128_f8f6f4 v[72:75], v[12:19], v[204:211], v[72:75], v219, v220 op_sel_hi:[0,0,0]
	v_mfma_scale_f32_16x16x128_f8f6f4 v[64:67], v[4:11], v[226:233], v[64:67], v219, v220 op_sel_hi:[0,0,0]
	v_mfma_scale_f32_16x16x128_f8f6f4 v[56:59], v[12:19], v[226:233], v[56:59], v219, v220 op_sel_hi:[0,0,0]
	v_mfma_scale_f32_16x16x128_f8f6f4 v[48:51], v[4:11], v[234:241], v[48:51], v219, v220 op_sel_hi:[0,0,0]
	v_mfma_scale_f32_16x16x128_f8f6f4 v[40:43], v[12:19], v[234:241], v[40:43], v219, v220 op_sel_hi:[0,0,0]
	s_setprio 0
	s_setprio 1
	v_mfma_scale_f32_16x16x128_f8f6f4 v[92:95], v[20:27], v[196:203], v[92:95], v219, v220 op_sel_hi:[0,0,0]
	v_mfma_scale_f32_16x16x128_f8f6f4 v[84:87], v[28:35], v[196:203], v[84:87], v219, v220 op_sel_hi:[0,0,0]
	v_mfma_scale_f32_16x16x128_f8f6f4 v[76:79], v[20:27], v[204:211], v[76:79], v219, v220 op_sel_hi:[0,0,0]
	v_mfma_scale_f32_16x16x128_f8f6f4 v[68:71], v[28:35], v[204:211], v[68:71], v219, v220 op_sel_hi:[0,0,0]
	v_mfma_scale_f32_16x16x128_f8f6f4 v[60:63], v[20:27], v[226:233], v[60:63], v219, v220 op_sel_hi:[0,0,0]
	v_mfma_scale_f32_16x16x128_f8f6f4 v[52:55], v[28:35], v[226:233], v[52:55], v219, v220 op_sel_hi:[0,0,0]
	v_mfma_scale_f32_16x16x128_f8f6f4 v[44:47], v[20:27], v[234:241], v[44:47], v219, v220 op_sel_hi:[0,0,0]
	v_mfma_scale_f32_16x16x128_f8f6f4 v[36:39], v[28:35], v[234:241], v[36:39], v219, v220 op_sel_hi:[0,0,0]
	s_setprio 0
	s_add_i32 s79, s79, 2
	s_add_u32 s52, s52, 0x100
	s_addc_u32 s53, s53, 0
	s_add_u32 s77, s77, 0x100
	s_addc_u32 s78, s78, 0
	s_cmp_gt_u32 s79, 13
	s_cbranch_scc1 .Lmy_kx_1812
	s_add_u32 s43, s52, 0xfffc0080
	s_addc_u32 s54, s53, -1
	s_add_i32 s42, 0, 0x10000
	s_cmp_eq_u32 s79, 12
	s_cselect_b32 s57, s10, s54
	s_cselect_b32 s56, s11, s43
	s_cselect_b32 s55, s39, s78
	s_cselect_b32 s54, s41, s77
	s_add_i32 s43, 0, 0x14000
	s_cmp_gt_u32 s79, 13
.Lmy_kx_1812:
	s_barrier
	s_cbranch_scc0 .Lmy_kl_1812
	s_nop 15
	s_nop 15
	s_and_b64 vcc, exec, s[36:37]
	v_readlane_b32 s78, v249, 36
	s_mov_b32 s79, s28
	s_cbranch_vccz .LBB0_1815
	s_barrier

.Lmy_kl_1894:
	ds_read_b128 v[20:23], v190
	ds_read_b128 v[28:31], v190 offset:2048
	ds_read_b128 v[24:27], v190 offset:1024
	ds_read_b128 v[32:35], v190 offset:3072
	ds_read_b128 v[4:7], v190 offset:16384
	ds_read_b128 v[12:15], v190 offset:18432
	ds_read_b128 v[8:11], v190 offset:17408
	ds_read_b128 v[16:19], v190 offset:19456
	v_lshl_add_u64 v[174:175], s[40:41], 0, v[170:171]
	s_add_i32 m0, s11, 0xc000
	ds_read_b128 v[178:181], v193
	ds_read_b128 v[196:199], v193 offset:2048
	ds_read_b128 v[182:185], v194
	ds_read_b128 v[200:203], v194 offset:2048
	ds_read_b128 v[204:207], v193 offset:4096
	ds_read_b128 v[226:229], v193 offset:6144
	ds_read_b128 v[208:211], v194 offset:4096
	ds_read_b128 v[230:233], v194 offset:6144
	global_load_lds_dwordx4 v[174:175], off
	v_lshl_add_u64 v[174:175], s[40:41], 0, v[172:173]
	s_add_i32 m0, s11, 0xe000
	s_nop 0
	global_load_lds_dwordx4 v[174:175], off
	s_waitcnt vmcnt(8)
	s_waitcnt lgkmcnt(0)
	s_barrier
	s_setprio 1
	s_waitcnt lgkmcnt(0)
	v_mfma_scale_f32_16x16x128_f8f6f4 v[160:163], v[20:27], v[178:185], v[160:163], v219, v220 op_sel_hi:[0,0,0]
	v_mfma_scale_f32_16x16x128_f8f6f4 v[156:159], v[28:35], v[178:185], v[156:159], v219, v220 op_sel_hi:[0,0,0]
	v_mfma_scale_f32_16x16x128_f8f6f4 v[152:155], v[20:27], v[196:203], v[152:155], v219, v220 op_sel_hi:[0,0,0]
	v_mfma_scale_f32_16x16x128_f8f6f4 v[148:151], v[28:35], v[196:203], v[148:151], v219, v220 op_sel_hi:[0,0,0]
	v_mfma_scale_f32_16x16x128_f8f6f4 v[136:139], v[20:27], v[204:211], v[136:139], v219, v220 op_sel_hi:[0,0,0]
	v_mfma_scale_f32_16x16x128_f8f6f4 v[132:135], v[28:35], v[204:211], v[132:135], v219, v220 op_sel_hi:[0,0,0]
	v_mfma_scale_f32_16x16x128_f8f6f4 v[120:123], v[20:27], v[226:233], v[120:123], v219, v220 op_sel_hi:[0,0,0]
	v_mfma_scale_f32_16x16x128_f8f6f4 v[116:119], v[28:35], v[226:233], v[116:119], v219, v220 op_sel_hi:[0,0,0]
	s_setprio 0
	s_setprio 1
	v_mfma_scale_f32_16x16x128_f8f6f4 v[144:147], v[4:11], v[178:185], v[144:147], v219, v220 op_sel_hi:[0,0,0]
	v_mfma_scale_f32_16x16x128_f8f6f4 v[140:143], v[12:19], v[178:185], v[140:143], v219, v220 op_sel_hi:[0,0,0]
	v_mfma_scale_f32_16x16x128_f8f6f4 v[128:131], v[4:11], v[196:203], v[128:131], v219, v220 op_sel_hi:[0,0,0]
	v_mfma_scale_f32_16x16x128_f8f6f4 v[124:127], v[12:19], v[196:203], v[124:127], v219, v220 op_sel_hi:[0,0,0]
	v_mfma_scale_f32_16x16x128_f8f6f4 v[112:115], v[4:11], v[204:211], v[112:115], v219, v220 op_sel_hi:[0,0,0]
	v_mfma_scale_f32_16x16x128_f8f6f4 v[108:111], v[12:19], v[204:211], v[108:111], v219, v220 op_sel_hi:[0,0,0]
	v_mfma_scale_f32_16x16x128_f8f6f4 v[104:107], v[4:11], v[226:233], v[104:107], v219, v220 op_sel_hi:[0,0,0]
	v_mfma_scale_f32_16x16x128_f8f6f4 v[100:103], v[12:19], v[226:233], v[100:103], v219, v220 op_sel_hi:[0,0,0]
	s_setprio 0
	s_barrier
	s_add_i32 s42, s42, s10
	v_lshl_add_u64 v[182:183], s[44:45], 0, v[2:3]
	s_mov_b32 m0, s42
	ds_read_b128 v[196:199], v193 offset:16384
	ds_read_b128 v[204:207], v193 offset:18432
	ds_read_b128 v[200:203], v194 offset:16384
	ds_read_b128 v[208:211], v194 offset:18432
	ds_read_b128 v[226:229], v193 offset:20480
	ds_read_b128 v[234:237], v193 offset:22528
	ds_read_b128 v[230:233], v194 offset:20480
	ds_read_b128 v[238:241], v194 offset:22528
	global_load_lds_dwordx4 v[182:183], off
	s_add_i32 m0, s42, 0x2000
	s_add_u32 s62, s44, 0xb0000
	v_lshl_add_u64 v[184:185], s[44:45], 0, v[164:165]
	s_addc_u32 s63, s45, 0
	s_add_i32 s42, s43, s10
	global_load_lds_dwordx4 v[184:185], off
	v_lshl_add_u64 v[174:175], s[62:63], 0, v[2:3]
	s_mov_b32 m0, s42
	v_lshl_add_u64 v[186:187], s[46:47], 0, v[168:169]
	global_load_lds_dwordx4 v[174:175], off
	v_lshl_add_u64 v[174:175], s[62:63], 0, v[164:165]
	s_add_i32 m0, s42, 0x2000
	v_lshl_add_u64 v[188:189], s[46:47], 0, v[166:167]
	global_load_lds_dwordx4 v[174:175], off
	s_mov_b32 m0, s11
	s_nop 0
	global_load_lds_dwordx4 v[186:187], off
	s_mov_b32 m0, s12
	s_nop 0
	global_load_lds_dwordx4 v[188:189], off
	s_waitcnt vmcnt(8)
	s_waitcnt lgkmcnt(0)
	s_barrier
	s_setprio 1
	s_waitcnt lgkmcnt(0)
	v_mfma_scale_f32_16x16x128_f8f6f4 v[96:99], v[20:27], v[196:203], v[96:99], v219, v220 op_sel_hi:[0,0,0]
	v_mfma_scale_f32_16x16x128_f8f6f4 v[92:95], v[28:35], v[196:203], v[92:95], v219, v220 op_sel_hi:[0,0,0]
	v_mfma_scale_f32_16x16x128_f8f6f4 v[88:91], v[20:27], v[204:211], v[88:91], v219, v220 op_sel_hi:[0,0,0]
	v_mfma_scale_f32_16x16x128_f8f6f4 v[84:87], v[28:35], v[204:211], v[84:87], v219, v220 op_sel_hi:[0,0,0]
	v_mfma_scale_f32_16x16x128_f8f6f4 v[72:75], v[20:27], v[226:233], v[72:75], v219, v220 op_sel_hi:[0,0,0]
	v_mfma_scale_f32_16x16x128_f8f6f4 v[68:71], v[28:35], v[226:233], v[68:71], v219, v220 op_sel_hi:[0,0,0]
	v_mfma_scale_f32_16x16x128_f8f6f4 v[56:59], v[20:27], v[234:241], v[56:59], v219, v220 op_sel_hi:[0,0,0]
	v_mfma_scale_f32_16x16x128_f8f6f4 v[52:55], v[28:35], v[234:241], v[52:55], v219, v220 op_sel_hi:[0,0,0]
	s_setprio 0
	s_setprio 1
	v_mfma_scale_f32_16x16x128_f8f6f4 v[80:83], v[4:11], v[196:203], v[80:83], v219, v220 op_sel_hi:[0,0,0]
	v_mfma_scale_f32_16x16x128_f8f6f4 v[76:79], v[12:19], v[196:203], v[76:79], v219, v220 op_sel_hi:[0,0,0]
	v_mfma_scale_f32_16x16x128_f8f6f4 v[64:67], v[4:11], v[204:211], v[64:67], v219, v220 op_sel_hi:[0,0,0]
	v_mfma_scale_f32_16x16x128_f8f6f4 v[60:63], v[12:19], v[204:211], v[60:63], v219, v220 op_sel_hi:[0,0,0]
	v_mfma_scale_f32_16x16x128_f8f6f4 v[48:51], v[4:11], v[226:233], v[48:51], v219, v220 op_sel_hi:[0,0,0]
	v_mfma_scale_f32_16x16x128_f8f6f4 v[44:47], v[12:19], v[226:233], v[44:47], v219, v220 op_sel_hi:[0,0,0]
	v_mfma_scale_f32_16x16x128_f8f6f4 v[40:43], v[4:11], v[234:241], v[40:43], v219, v220 op_sel_hi:[0,0,0]
	v_mfma_scale_f32_16x16x128_f8f6f4 v[36:39], v[12:19], v[234:241], v[36:39], v219, v220 op_sel_hi:[0,0,0]
	s_setprio 0
	s_barrier
	s_add_i32 s62, 0, 0x18000
	s_add_i32 s63, 0, 0x1c000
	ds_read_b128 v[4:7], v190 offset:32768
	ds_read_b128 v[12:15], v190 offset:34816
	ds_read_b128 v[8:11], v190 offset:33792
	ds_read_b128 v[16:19], v190 offset:35840
	ds_read_b128 v[20:23], v190 offset:49152
	ds_read_b128 v[28:31], v190 offset:51200
	ds_read_b128 v[24:27], v190 offset:50176
	ds_read_b128 v[32:35], v190 offset:52224
	s_add_u32 s42, s46, 0xb0000
	s_addc_u32 s43, s47, 0
	s_mov_b32 m0, s48
	v_lshl_add_u64 v[174:175], s[42:43], 0, v[168:169]
	ds_read_b128 v[196:199], v193 offset:32768
	ds_read_b128 v[204:207], v193 offset:34816
	ds_read_b128 v[200:203], v194 offset:32768
	ds_read_b128 v[208:211], v194 offset:34816
	ds_read_b128 v[226:229], v193 offset:36864
	ds_read_b128 v[234:237], v193 offset:38912
	ds_read_b128 v[230:233], v194 offset:36864
	ds_read_b128 v[238:241], v194 offset:38912
	global_load_lds_dwordx4 v[174:175], off
	v_lshl_add_u64 v[174:175], s[42:43], 0, v[166:167]
	s_mov_b32 m0, s49
	s_nop 0
	global_load_lds_dwordx4 v[174:175], off
	s_waitcnt vmcnt(8)
	s_waitcnt lgkmcnt(0)
	s_barrier
	s_setprio 1
	s_waitcnt lgkmcnt(0)
	v_mfma_scale_f32_16x16x128_f8f6f4 v[160:163], v[4:11], v[196:203], v[160:163], v219, v220 op_sel_hi:[0,0,0]
	v_mfma_scale_f32_16x16x128_f8f6f4 v[156:159], v[12:19], v[196:203], v[156:159], v219, v220 op_sel_hi:[0,0,0]
	v_mfma_scale_f32_16x16x128_f8f6f4 v[152:155], v[4:11], v[204:211], v[152:155], v219, v220 op_sel_hi:[0,0,0]
	v_mfma_scale_f32_16x16x128_f8f6f4 v[148:151], v[12:19], v[204:211], v[148:151], v219, v220 op_sel_hi:[0,0,0]
	v_mfma_scale_f32_16x16x128_f8f6f4 v[136:139], v[4:11], v[226:233], v[136:139], v219, v220 op_sel_hi:[0,0,0]
	v_mfma_scale_f32_16x16x128_f8f6f4 v[132:135], v[12:19], v[226:233], v[132:135], v219, v220 op_sel_hi:[0,0,0]
	v_mfma_scale_f32_16x16x128_f8f6f4 v[120:123], v[4:11], v[234:241], v[120:123], v219, v220 op_sel_hi:[0,0,0]
	v_mfma_scale_f32_16x16x128_f8f6f4 v[116:119], v[12:19], v[234:241], v[116:119], v219, v220 op_sel_hi:[0,0,0]
	s_setprio 0
	s_setprio 1
	v_mfma_scale_f32_16x16x128_f8f6f4 v[144:147], v[20:27], v[196:203], v[144:147], v219, v220 op_sel_hi:[0,0,0]
	v_mfma_scale_f32_16x16x128_f8f6f4 v[140:143], v[28:35], v[196:203], v[140:143], v219, v220 op_sel_hi:[0,0,0]
	v_mfma_scale_f32_16x16x128_f8f6f4 v[128:131], v[20:27], v[204:211], v[128:131], v219, v220 op_sel_hi:[0,0,0]
	v_mfma_scale_f32_16x16x128_f8f6f4 v[124:127], v[28:35], v[204:211], v[124:127], v219, v220 op_sel_hi:[0,0,0]
	v_mfma_scale_f32_16x16x128_f8f6f4 v[112:115], v[20:27], v[226:233], v[112:115], v219, v220 op_sel_hi:[0,0,0]
	v_mfma_scale_f32_16x16x128_f8f6f4 v[108:111], v[28:35], v[226:233], v[108:111], v219, v220 op_sel_hi:[0,0,0]
	v_mfma_scale_f32_16x16x128_f8f6f4 v[104:107], v[20:27], v[234:241], v[104:107], v219, v220 op_sel_hi:[0,0,0]
	v_mfma_scale_f32_16x16x128_f8f6f4 v[100:103], v[28:35], v[234:241], v[100:103], v219, v220 op_sel_hi:[0,0,0]
	s_setprio 0
	s_barrier
	s_add_i32 s42, s62, s10
	v_lshl_add_u64 v[174:175], v[182:183], 0, s[6:7]
	s_mov_b32 m0, s42
	ds_read_b128 v[196:199], v193 offset:49152
	ds_read_b128 v[204:207], v193 offset:51200
	ds_read_b128 v[200:203], v194 offset:49152
	ds_read_b128 v[208:211], v194 offset:51200
	ds_read_b128 v[226:229], v193 offset:53248
	ds_read_b128 v[234:237], v193 offset:55296
	ds_read_b128 v[230:233], v194 offset:53248
	ds_read_b128 v[238:241], v194 offset:55296
	global_load_lds_dwordx4 v[174:175], off
	s_add_i32 m0, s42, 0x2000
	s_add_u32 s42, s44, 0xb0080
	v_lshl_add_u64 v[174:175], v[184:185], 0, s[6:7]
	s_addc_u32 s43, s45, 0
	s_add_i32 s44, s63, s10
	global_load_lds_dwordx4 v[174:175], off
	v_lshl_add_u64 v[174:175], s[42:43], 0, v[2:3]
	s_mov_b32 m0, s44
	s_nop 0
	global_load_lds_dwordx4 v[174:175], off
	v_lshl_add_u64 v[174:175], s[42:43], 0, v[164:165]
	s_add_i32 m0, s44, 0x2000
	s_nop 0
	global_load_lds_dwordx4 v[174:175], off
	v_lshl_add_u64 v[174:175], v[186:187], 0, s[6:7]
	s_mov_b32 m0, s52
	s_nop 0
	global_load_lds_dwordx4 v[174:175], off
	v_lshl_add_u64 v[174:175], v[188:189], 0, s[6:7]
	s_mov_b32 m0, s53
	s_nop 0
	global_load_lds_dwordx4 v[174:175], off
	s_waitcnt vmcnt(8)
	s_waitcnt lgkmcnt(0)
	s_barrier
	s_setprio 1
	s_waitcnt lgkmcnt(0)
	v_mfma_scale_f32_16x16x128_f8f6f4 v[96:99], v[4:11], v[196:203], v[96:99], v219, v220 op_sel_hi:[0,0,0]
	v_mfma_scale_f32_16x16x128_f8f6f4 v[92:95], v[12:19], v[196:203], v[92:95], v219, v220 op_sel_hi:[0,0,0]
	v_mfma_scale_f32_16x16x128_f8f6f4 v[88:91], v[4:11], v[204:211], v[88:91], v219, v220 op_sel_hi:[0,0,0]
	v_mfma_scale_f32_16x16x128_f8f6f4 v[84:87], v[12:19], v[204:211], v[84:87], v219, v220 op_sel_hi:[0,0,0]
	v_mfma_scale_f32_16x16x128_f8f6f4 v[72:75], v[4:11], v[226:233], v[72:75], v219, v220 op_sel_hi:[0,0,0]
	v_mfma_scale_f32_16x16x128_f8f6f4 v[68:71], v[12:19], v[226:233], v[68:71], v219, v220 op_sel_hi:[0,0,0]
	v_mfma_scale_f32_16x16x128_f8f6f4 v[56:59], v[4:11], v[234:241], v[56:59], v219, v220 op_sel_hi:[0,0,0]
	v_mfma_scale_f32_16x16x128_f8f6f4 v[52:55], v[12:19], v[234:241], v[52:55], v219, v220 op_sel_hi:[0,0,0]
	s_setprio 0
	s_setprio 1
	v_mfma_scale_f32_16x16x128_f8f6f4 v[80:83], v[20:27], v[196:203], v[80:83], v219, v220 op_sel_hi:[0,0,0]
	v_mfma_scale_f32_16x16x128_f8f6f4 v[76:79], v[28:35], v[196:203], v[76:79], v219, v220 op_sel_hi:[0,0,0]
	v_mfma_scale_f32_16x16x128_f8f6f4 v[64:67], v[20:27], v[204:211], v[64:67], v219, v220 op_sel_hi:[0,0,0]
	v_mfma_scale_f32_16x16x128_f8f6f4 v[60:63], v[28:35], v[204:211], v[60:63], v219, v220 op_sel_hi:[0,0,0]
	v_mfma_scale_f32_16x16x128_f8f6f4 v[48:51], v[20:27], v[226:233], v[48:51], v219, v220 op_sel_hi:[0,0,0]
	v_mfma_scale_f32_16x16x128_f8f6f4 v[44:47], v[28:35], v[226:233], v[44:47], v219, v220 op_sel_hi:[0,0,0]
	v_mfma_scale_f32_16x16x128_f8f6f4 v[40:43], v[20:27], v[234:241], v[40:43], v219, v220 op_sel_hi:[0,0,0]
	v_mfma_scale_f32_16x16x128_f8f6f4 v[36:39], v[28:35], v[234:241], v[36:39], v219, v220 op_sel_hi:[0,0,0]
	s_setprio 0
	s_add_i32 s61, s61, 2
	s_add_u32 s40, s40, 0x100
	s_addc_u32 s41, s41, 0
	s_add_u32 s59, s59, 0x100
	s_addc_u32 s60, s60, 0
	s_cmp_gt_u32 s61, 41
	s_cbranch_scc1 .Lmy_kx_1894
	s_add_u32 s43, s40, 0xfff50080
	s_addc_u32 s44, s41, -1
	s_add_i32 s42, 0, 0x10000
	s_cmp_eq_u32 s61, 40
	s_cselect_b32 s47, s5, s44
	s_cselect_b32 s46, s4, s43
	s_cselect_b32 s45, s39, s60
	s_cselect_b32 s44, s38, s59
	s_add_i32 s43, 0, 0x14000
	s_cmp_gt_u32 s61, 41
.Lmy_kx_1894:
	s_barrier
	s_cbranch_scc0 .Lmy_kl_1894
	s_nop 15
	s_nop 15
	s_and_b64 vcc, exec, s[36:37]
	s_cbranch_vccz .LBB0_1897
	s_barrier

.Lmy_kl_1948:
	ds_read_b128 v[20:23], v190
	ds_read_b128 v[28:31], v190 offset:2048
	ds_read_b128 v[24:27], v190 offset:1024
	ds_read_b128 v[32:35], v190 offset:3072
	ds_read_b128 v[4:7], v190 offset:16384
	ds_read_b128 v[12:15], v190 offset:18432
	ds_read_b128 v[8:11], v190 offset:17408
	ds_read_b128 v[16:19], v190 offset:19456
	v_lshl_add_u64 v[174:175], s[44:45], 0, v[170:171]
	s_add_i32 m0, s59, 0xc000
	ds_read_b128 v[178:181], v193
	ds_read_b128 v[196:199], v193 offset:2048
	ds_read_b128 v[182:185], v194
	ds_read_b128 v[200:203], v194 offset:2048
	ds_read_b128 v[204:207], v193 offset:4096
	ds_read_b128 v[226:229], v193 offset:6144
	ds_read_b128 v[208:211], v194 offset:4096
	ds_read_b128 v[230:233], v194 offset:6144
	global_load_lds_dwordx4 v[174:175], off
	v_lshl_add_u64 v[174:175], s[44:45], 0, v[172:173]
	s_add_i32 m0, s59, 0xe000
	s_nop 0
	global_load_lds_dwordx4 v[174:175], off
	s_waitcnt vmcnt(8)
	s_waitcnt lgkmcnt(0)
	s_barrier
	s_setprio 1
	s_waitcnt lgkmcnt(0)
	v_mfma_scale_f32_16x16x128_f8f6f4 v[160:163], v[20:27], v[178:185], v[160:163], v219, v220 op_sel_hi:[0,0,0]
	v_mfma_scale_f32_16x16x128_f8f6f4 v[156:159], v[28:35], v[178:185], v[156:159], v219, v220 op_sel_hi:[0,0,0]
	v_mfma_scale_f32_16x16x128_f8f6f4 v[152:155], v[20:27], v[196:203], v[152:155], v219, v220 op_sel_hi:[0,0,0]
	v_mfma_scale_f32_16x16x128_f8f6f4 v[148:151], v[28:35], v[196:203], v[148:151], v219, v220 op_sel_hi:[0,0,0]
	v_mfma_scale_f32_16x16x128_f8f6f4 v[136:139], v[20:27], v[204:211], v[136:139], v219, v220 op_sel_hi:[0,0,0]
	v_mfma_scale_f32_16x16x128_f8f6f4 v[132:135], v[28:35], v[204:211], v[132:135], v219, v220 op_sel_hi:[0,0,0]
	v_mfma_scale_f32_16x16x128_f8f6f4 v[120:123], v[20:27], v[226:233], v[120:123], v219, v220 op_sel_hi:[0,0,0]
	v_mfma_scale_f32_16x16x128_f8f6f4 v[116:119], v[28:35], v[226:233], v[116:119], v219, v220 op_sel_hi:[0,0,0]
	s_setprio 0
	s_setprio 1
	v_mfma_scale_f32_16x16x128_f8f6f4 v[144:147], v[4:11], v[178:185], v[144:147], v219, v220 op_sel_hi:[0,0,0]
	v_mfma_scale_f32_16x16x128_f8f6f4 v[140:143], v[12:19], v[178:185], v[140:143], v219, v220 op_sel_hi:[0,0,0]
	v_mfma_scale_f32_16x16x128_f8f6f4 v[128:131], v[4:11], v[196:203], v[128:131], v219, v220 op_sel_hi:[0,0,0]
	v_mfma_scale_f32_16x16x128_f8f6f4 v[124:127], v[12:19], v[196:203], v[124:127], v219, v220 op_sel_hi:[0,0,0]
	v_mfma_scale_f32_16x16x128_f8f6f4 v[112:115], v[4:11], v[204:211], v[112:115], v219, v220 op_sel_hi:[0,0,0]
	v_mfma_scale_f32_16x16x128_f8f6f4 v[108:111], v[12:19], v[204:211], v[108:111], v219, v220 op_sel_hi:[0,0,0]
	v_mfma_scale_f32_16x16x128_f8f6f4 v[104:107], v[4:11], v[226:233], v[104:107], v219, v220 op_sel_hi:[0,0,0]
	v_mfma_scale_f32_16x16x128_f8f6f4 v[100:103], v[12:19], v[226:233], v[100:103], v219, v220 op_sel_hi:[0,0,0]
	s_setprio 0
	s_barrier
	s_add_i32 s42, s42, s55
	v_lshl_add_u64 v[182:183], s[46:47], 0, v[2:3]
	s_mov_b32 m0, s42
	ds_read_b128 v[196:199], v193 offset:16384
	ds_read_b128 v[204:207], v193 offset:18432
	ds_read_b128 v[200:203], v194 offset:16384
	ds_read_b128 v[208:211], v194 offset:18432
	ds_read_b128 v[226:229], v193 offset:20480
	ds_read_b128 v[234:237], v193 offset:22528
	ds_read_b128 v[230:233], v194 offset:20480
	ds_read_b128 v[238:241], v194 offset:22528
	global_load_lds_dwordx4 v[182:183], off
	s_add_i32 m0, s42, 0x2000
	s_add_u32 s74, s46, 0x58000
	v_lshl_add_u64 v[184:185], s[46:47], 0, v[164:165]
	s_addc_u32 s75, s47, 0
	s_add_i32 s42, s43, s55
	global_load_lds_dwordx4 v[184:185], off
	v_lshl_add_u64 v[174:175], s[74:75], 0, v[2:3]
	s_mov_b32 m0, s42
	v_lshl_add_u64 v[186:187], s[48:49], 0, v[168:169]
	global_load_lds_dwordx4 v[174:175], off
	v_lshl_add_u64 v[174:175], s[74:75], 0, v[164:165]
	s_add_i32 m0, s42, 0x2000
	v_lshl_add_u64 v[188:189], s[48:49], 0, v[166:167]
	global_load_lds_dwordx4 v[174:175], off
	s_mov_b32 m0, s59
	s_nop 0
	global_load_lds_dwordx4 v[186:187], off
	s_mov_b32 m0, s60
	s_nop 0
	global_load_lds_dwordx4 v[188:189], off
	s_waitcnt vmcnt(8)
	s_waitcnt lgkmcnt(0)
	s_barrier
	s_setprio 1
	s_waitcnt lgkmcnt(0)
	v_mfma_scale_f32_16x16x128_f8f6f4 v[96:99], v[20:27], v[196:203], v[96:99], v219, v220 op_sel_hi:[0,0,0]
	v_mfma_scale_f32_16x16x128_f8f6f4 v[92:95], v[28:35], v[196:203], v[92:95], v219, v220 op_sel_hi:[0,0,0]
	v_mfma_scale_f32_16x16x128_f8f6f4 v[88:91], v[20:27], v[204:211], v[88:91], v219, v220 op_sel_hi:[0,0,0]
	v_mfma_scale_f32_16x16x128_f8f6f4 v[84:87], v[28:35], v[204:211], v[84:87], v219, v220 op_sel_hi:[0,0,0]
	v_mfma_scale_f32_16x16x128_f8f6f4 v[72:75], v[20:27], v[226:233], v[72:75], v219, v220 op_sel_hi:[0,0,0]
	v_mfma_scale_f32_16x16x128_f8f6f4 v[68:71], v[28:35], v[226:233], v[68:71], v219, v220 op_sel_hi:[0,0,0]
	v_mfma_scale_f32_16x16x128_f8f6f4 v[56:59], v[20:27], v[234:241], v[56:59], v219, v220 op_sel_hi:[0,0,0]
	v_mfma_scale_f32_16x16x128_f8f6f4 v[52:55], v[28:35], v[234:241], v[52:55], v219, v220 op_sel_hi:[0,0,0]
	s_setprio 0
	s_setprio 1
	v_mfma_scale_f32_16x16x128_f8f6f4 v[80:83], v[4:11], v[196:203], v[80:83], v219, v220 op_sel_hi:[0,0,0]
	v_mfma_scale_f32_16x16x128_f8f6f4 v[76:79], v[12:19], v[196:203], v[76:79], v219, v220 op_sel_hi:[0,0,0]
	v_mfma_scale_f32_16x16x128_f8f6f4 v[64:67], v[4:11], v[204:211], v[64:67], v219, v220 op_sel_hi:[0,0,0]
	v_mfma_scale_f32_16x16x128_f8f6f4 v[60:63], v[12:19], v[204:211], v[60:63], v219, v220 op_sel_hi:[0,0,0]
	v_mfma_scale_f32_16x16x128_f8f6f4 v[48:51], v[4:11], v[226:233], v[48:51], v219, v220 op_sel_hi:[0,0,0]
	v_mfma_scale_f32_16x16x128_f8f6f4 v[44:47], v[12:19], v[226:233], v[44:47], v219, v220 op_sel_hi:[0,0,0]
	v_mfma_scale_f32_16x16x128_f8f6f4 v[40:43], v[4:11], v[234:241], v[40:43], v219, v220 op_sel_hi:[0,0,0]
	v_mfma_scale_f32_16x16x128_f8f6f4 v[36:39], v[12:19], v[234:241], v[36:39], v219, v220 op_sel_hi:[0,0,0]
	s_setprio 0
	s_barrier
	s_add_i32 s73, 0, 0x18000
	s_add_i32 s74, 0, 0x1c000
	ds_read_b128 v[4:7], v190 offset:32768
	ds_read_b128 v[12:15], v190 offset:34816
	ds_read_b128 v[8:11], v190 offset:33792
	ds_read_b128 v[16:19], v190 offset:35840
	ds_read_b128 v[20:23], v190 offset:49152
	ds_read_b128 v[28:31], v190 offset:51200
	ds_read_b128 v[24:27], v190 offset:50176
	ds_read_b128 v[32:35], v190 offset:52224
	s_add_u32 s42, s48, 0x58000
	s_addc_u32 s43, s49, 0
	s_mov_b32 m0, s61
	v_lshl_add_u64 v[174:175], s[42:43], 0, v[168:169]
	ds_read_b128 v[196:199], v193 offset:32768
	ds_read_b128 v[204:207], v193 offset:34816
	ds_read_b128 v[200:203], v194 offset:32768
	ds_read_b128 v[208:211], v194 offset:34816
	ds_read_b128 v[226:229], v193 offset:36864
	ds_read_b128 v[234:237], v193 offset:38912
	ds_read_b128 v[230:233], v194 offset:36864
	ds_read_b128 v[238:241], v194 offset:38912
	global_load_lds_dwordx4 v[174:175], off
	v_lshl_add_u64 v[174:175], s[42:43], 0, v[166:167]
	s_mov_b32 m0, s62
	s_nop 0
	global_load_lds_dwordx4 v[174:175], off
	s_waitcnt vmcnt(8)
	s_waitcnt lgkmcnt(0)
	s_barrier
	s_setprio 1
	s_waitcnt lgkmcnt(0)
	v_mfma_scale_f32_16x16x128_f8f6f4 v[160:163], v[4:11], v[196:203], v[160:163], v219, v220 op_sel_hi:[0,0,0]
	v_mfma_scale_f32_16x16x128_f8f6f4 v[156:159], v[12:19], v[196:203], v[156:159], v219, v220 op_sel_hi:[0,0,0]
	v_mfma_scale_f32_16x16x128_f8f6f4 v[152:155], v[4:11], v[204:211], v[152:155], v219, v220 op_sel_hi:[0,0,0]
	v_mfma_scale_f32_16x16x128_f8f6f4 v[148:151], v[12:19], v[204:211], v[148:151], v219, v220 op_sel_hi:[0,0,0]
	v_mfma_scale_f32_16x16x128_f8f6f4 v[136:139], v[4:11], v[226:233], v[136:139], v219, v220 op_sel_hi:[0,0,0]
	v_mfma_scale_f32_16x16x128_f8f6f4 v[132:135], v[12:19], v[226:233], v[132:135], v219, v220 op_sel_hi:[0,0,0]
	v_mfma_scale_f32_16x16x128_f8f6f4 v[120:123], v[4:11], v[234:241], v[120:123], v219, v220 op_sel_hi:[0,0,0]
	v_mfma_scale_f32_16x16x128_f8f6f4 v[116:119], v[12:19], v[234:241], v[116:119], v219, v220 op_sel_hi:[0,0,0]
	s_setprio 0
	s_setprio 1
	v_mfma_scale_f32_16x16x128_f8f6f4 v[144:147], v[20:27], v[196:203], v[144:147], v219, v220 op_sel_hi:[0,0,0]
	v_mfma_scale_f32_16x16x128_f8f6f4 v[140:143], v[28:35], v[196:203], v[140:143], v219, v220 op_sel_hi:[0,0,0]
	v_mfma_scale_f32_16x16x128_f8f6f4 v[128:131], v[20:27], v[204:211], v[128:131], v219, v220 op_sel_hi:[0,0,0]
	v_mfma_scale_f32_16x16x128_f8f6f4 v[124:127], v[28:35], v[204:211], v[124:127], v219, v220 op_sel_hi:[0,0,0]
	v_mfma_scale_f32_16x16x128_f8f6f4 v[112:115], v[20:27], v[226:233], v[112:115], v219, v220 op_sel_hi:[0,0,0]
	v_mfma_scale_f32_16x16x128_f8f6f4 v[108:111], v[28:35], v[226:233], v[108:111], v219, v220 op_sel_hi:[0,0,0]
	v_mfma_scale_f32_16x16x128_f8f6f4 v[104:107], v[20:27], v[234:241], v[104:107], v219, v220 op_sel_hi:[0,0,0]
	v_mfma_scale_f32_16x16x128_f8f6f4 v[100:103], v[28:35], v[234:241], v[100:103], v219, v220 op_sel_hi:[0,0,0]
	s_setprio 0
	s_barrier
	s_add_i32 s42, s73, s55
	v_lshl_add_u64 v[174:175], v[182:183], 0, s[6:7]
	s_mov_b32 m0, s42
	ds_read_b128 v[196:199], v193 offset:49152
	ds_read_b128 v[204:207], v193 offset:51200
	ds_read_b128 v[200:203], v194 offset:49152
	ds_read_b128 v[208:211], v194 offset:51200
	ds_read_b128 v[226:229], v193 offset:53248
	ds_read_b128 v[234:237], v193 offset:55296
	ds_read_b128 v[230:233], v194 offset:53248
	ds_read_b128 v[238:241], v194 offset:55296
	global_load_lds_dwordx4 v[174:175], off
	s_add_i32 m0, s42, 0x2000
	s_add_u32 s42, s46, 0x58080
	v_lshl_add_u64 v[174:175], v[184:185], 0, s[6:7]
	s_addc_u32 s43, s47, 0
	s_add_i32 s46, s74, s55
	global_load_lds_dwordx4 v[174:175], off
	v_lshl_add_u64 v[174:175], s[42:43], 0, v[2:3]
	s_mov_b32 m0, s46
	s_nop 0
	global_load_lds_dwordx4 v[174:175], off
	v_lshl_add_u64 v[174:175], s[42:43], 0, v[164:165]
	s_add_i32 m0, s46, 0x2000
	s_nop 0
	global_load_lds_dwordx4 v[174:175], off
	v_lshl_add_u64 v[174:175], v[186:187], 0, s[6:7]
	s_mov_b32 m0, s64
	s_nop 0
	global_load_lds_dwordx4 v[174:175], off
	v_lshl_add_u64 v[174:175], v[188:189], 0, s[6:7]
	s_mov_b32 m0, s65
	s_nop 0
	global_load_lds_dwordx4 v[174:175], off
	s_waitcnt vmcnt(8)
	s_waitcnt lgkmcnt(0)
	s_barrier
	s_setprio 1
	s_waitcnt lgkmcnt(0)
	v_mfma_scale_f32_16x16x128_f8f6f4 v[96:99], v[4:11], v[196:203], v[96:99], v219, v220 op_sel_hi:[0,0,0]
	v_mfma_scale_f32_16x16x128_f8f6f4 v[92:95], v[12:19], v[196:203], v[92:95], v219, v220 op_sel_hi:[0,0,0]
	v_mfma_scale_f32_16x16x128_f8f6f4 v[88:91], v[4:11], v[204:211], v[88:91], v219, v220 op_sel_hi:[0,0,0]
	v_mfma_scale_f32_16x16x128_f8f6f4 v[84:87], v[12:19], v[204:211], v[84:87], v219, v220 op_sel_hi:[0,0,0]
	v_mfma_scale_f32_16x16x128_f8f6f4 v[72:75], v[4:11], v[226:233], v[72:75], v219, v220 op_sel_hi:[0,0,0]
	v_mfma_scale_f32_16x16x128_f8f6f4 v[68:71], v[12:19], v[226:233], v[68:71], v219, v220 op_sel_hi:[0,0,0]
	v_mfma_scale_f32_16x16x128_f8f6f4 v[56:59], v[4:11], v[234:241], v[56:59], v219, v220 op_sel_hi:[0,0,0]
	v_mfma_scale_f32_16x16x128_f8f6f4 v[52:55], v[12:19], v[234:241], v[52:55], v219, v220 op_sel_hi:[0,0,0]
	s_setprio 0
	s_setprio 1
	v_mfma_scale_f32_16x16x128_f8f6f4 v[80:83], v[20:27], v[196:203], v[80:83], v219, v220 op_sel_hi:[0,0,0]
	v_mfma_scale_f32_16x16x128_f8f6f4 v[76:79], v[28:35], v[196:203], v[76:79], v219, v220 op_sel_hi:[0,0,0]
	v_mfma_scale_f32_16x16x128_f8f6f4 v[64:67], v[20:27], v[204:211], v[64:67], v219, v220 op_sel_hi:[0,0,0]
	v_mfma_scale_f32_16x16x128_f8f6f4 v[60:63], v[28:35], v[204:211], v[60:63], v219, v220 op_sel_hi:[0,0,0]
	v_mfma_scale_f32_16x16x128_f8f6f4 v[48:51], v[20:27], v[226:233], v[48:51], v219, v220 op_sel_hi:[0,0,0]
	v_mfma_scale_f32_16x16x128_f8f6f4 v[44:47], v[28:35], v[226:233], v[44:47], v219, v220 op_sel_hi:[0,0,0]
	v_mfma_scale_f32_16x16x128_f8f6f4 v[40:43], v[20:27], v[234:241], v[40:43], v219, v220 op_sel_hi:[0,0,0]
	v_mfma_scale_f32_16x16x128_f8f6f4 v[36:39], v[28:35], v[234:241], v[36:39], v219, v220 op_sel_hi:[0,0,0]
	s_setprio 0
	s_add_i32 s72, s72, 2
	s_add_u32 s44, s44, 0x100
	s_addc_u32 s45, s45, 0
	s_add_u32 s70, s70, 0x100
	s_addc_u32 s71, s71, 0
	s_cmp_gt_u32 s72, 19
	s_cbranch_scc1 .Lmy_kx_1948
	s_add_u32 s43, s44, 0xfffa8080
	s_addc_u32 s46, s45, -1
	s_add_i32 s42, 0, 0x10000
	s_cmp_eq_u32 s72, 18
	s_cselect_b32 s49, s5, s46
	s_cselect_b32 s48, s4, s43
	s_cselect_b32 s47, s41, s71
	s_cselect_b32 s46, s40, s70
	s_add_i32 s43, 0, 0x14000
	s_cmp_gt_u32 s72, 19
.Lmy_kx_1948:
	s_barrier
	s_cbranch_scc0 .Lmy_kl_1948
	s_nop 15
	s_nop 15
	s_and_b64 vcc, exec, s[38:39]
	s_cbranch_vccz .LBB0_1951
	s_barrier
